# speedup vs baseline: 1.0040x; 1.0012x over previous
_Z11attn_kernelPKfiPDF16_S1_iii:
	s_bitcmp1_b32 s3, 0
	s_cbranch_scc0 .Lprio_skip_q0
	s_setprio 1
.Lprio_skip_q0:
	s_load_dwordx4 s[20:23], s[0:1], 0x20
	v_mov_b32_e32 v1, 0x2200
	v_lshl_or_b32 v1, v0, 2, v1
	s_mov_b32 s11, 0
	s_waitcnt lgkmcnt(0)
	s_cmp_gt_i32 s20, 0
	s_cselect_b64 s[28:29], -1, 0
	s_cmp_lt_i32 s20, 1
	s_cbranch_scc1 .LBB4_11
	s_load_dword s10, s[0:1], 0x8
	s_load_dwordx2 s[4:5], s[0:1], 0x0
	v_lshlrev_b32_e32 v2, 2, v0
	v_add_u32_e32 v3, 0x1000, v2
	s_waitcnt lgkmcnt(0)
	s_mul_i32 s10, s10, s2
	s_mul_i32 s10, s10, 0x1800
	s_lshl_b32 s6, s3, 8
	s_add_u32 s10, s10, s6
	s_add_u32 s40, s4, s10
	s_addc_u32 s41, s5, 0
	global_load_dword v50, v2, s[40:41]
	global_load_dword v51, v2, s[40:41] offset:2048
	global_load_dword v52, v3, s[40:41]
	s_cmp_le_i32 s20, 1
	s_cbranch_scc1 .Lattn_fill_wait
	s_add_u32 s40, s40, 0x1800
	s_addc_u32 s41, s41, 0
	global_load_dword v53, v2, s[40:41]
	global_load_dword v54, v2, s[40:41] offset:2048
	global_load_dword v55, v3, s[40:41]
	s_cmp_le_i32 s20, 2
	s_cbranch_scc1 .Lattn_fill_wait
	s_add_u32 s40, s40, 0x1800
	s_addc_u32 s41, s41, 0
	global_load_dword v56, v2, s[40:41]
	global_load_dword v57, v2, s[40:41] offset:2048
	global_load_dword v58, v3, s[40:41]
	s_cmp_le_i32 s20, 3
	s_cbranch_scc1 .Lattn_fill_wait
	s_add_u32 s40, s40, 0x1800
	s_addc_u32 s41, s41, 0
	global_load_dword v59, v2, s[40:41]
	global_load_dword v60, v2, s[40:41] offset:2048
	global_load_dword v61, v3, s[40:41]
	s_cmp_le_i32 s20, 4
	s_cbranch_scc1 .Lattn_fill_wait
	s_add_u32 s40, s40, 0x1800
	s_addc_u32 s41, s41, 0
	global_load_dword v62, v2, s[40:41]
	global_load_dword v63, v2, s[40:41] offset:2048
	global_load_dword v64, v3, s[40:41]
	s_cmp_le_i32 s20, 5
	s_cbranch_scc1 .Lattn_fill_wait
	s_add_u32 s40, s40, 0x1800
	s_addc_u32 s41, s41, 0
	global_load_dword v65, v2, s[40:41]
	global_load_dword v66, v2, s[40:41] offset:2048
	global_load_dword v67, v3, s[40:41]
	s_cmp_le_i32 s20, 6
	s_cbranch_scc1 .Lattn_fill_wait
	s_add_u32 s40, s40, 0x1800
	s_addc_u32 s41, s41, 0
	global_load_dword v68, v2, s[40:41]
	global_load_dword v69, v2, s[40:41] offset:2048
	global_load_dword v70, v3, s[40:41]
	s_cmp_le_i32 s20, 7
	s_cbranch_scc1 .Lattn_fill_wait
	s_add_u32 s40, s40, 0x1800
	s_addc_u32 s41, s41, 0
	global_load_dword v71, v2, s[40:41]
	global_load_dword v72, v2, s[40:41] offset:2048
	global_load_dword v73, v3, s[40:41]
	s_cmp_le_i32 s20, 8
	s_cbranch_scc1 .Lattn_fill_wait
	s_add_u32 s40, s40, 0x1800
	s_addc_u32 s41, s41, 0
	global_load_dword v74, v2, s[40:41]
	global_load_dword v75, v2, s[40:41] offset:2048
	global_load_dword v76, v3, s[40:41]
	s_cmp_le_i32 s20, 9
	s_cbranch_scc1 .Lattn_fill_wait
	s_add_u32 s40, s40, 0x1800
	s_addc_u32 s41, s41, 0
	global_load_dword v77, v2, s[40:41]
	global_load_dword v78, v2, s[40:41] offset:2048
	global_load_dword v79, v3, s[40:41]
	s_cmp_le_i32 s20, 10
	s_cbranch_scc1 .Lattn_fill_wait
	s_add_u32 s40, s40, 0x1800
	s_addc_u32 s41, s41, 0
	global_load_dword v80, v2, s[40:41]
	global_load_dword v81, v2, s[40:41] offset:2048
	global_load_dword v82, v3, s[40:41]
	s_cmp_le_i32 s20, 11
	s_cbranch_scc1 .Lattn_fill_wait
	s_add_u32 s40, s40, 0x1800
	s_addc_u32 s41, s41, 0
	global_load_dword v83, v2, s[40:41]
	global_load_dword v84, v2, s[40:41] offset:2048
	global_load_dword v85, v3, s[40:41]
	s_cmp_le_i32 s20, 12
	s_cbranch_scc1 .Lattn_fill_wait
	s_add_u32 s40, s40, 0x1800
	s_addc_u32 s41, s41, 0
	global_load_dword v86, v2, s[40:41]
	global_load_dword v87, v2, s[40:41] offset:2048
	global_load_dword v88, v3, s[40:41]
	s_cmp_le_i32 s20, 13
	s_cbranch_scc1 .Lattn_fill_wait
	s_add_u32 s40, s40, 0x1800
	s_addc_u32 s41, s41, 0
	global_load_dword v89, v2, s[40:41]
	global_load_dword v90, v2, s[40:41] offset:2048
	global_load_dword v91, v3, s[40:41]
	s_cmp_le_i32 s20, 14
	s_cbranch_scc1 .Lattn_fill_wait
	s_add_u32 s40, s40, 0x1800
	s_addc_u32 s41, s41, 0
	global_load_dword v92, v2, s[40:41]
	global_load_dword v93, v2, s[40:41] offset:2048
	global_load_dword v94, v3, s[40:41]
	s_cmp_le_i32 s20, 15
	s_cbranch_scc1 .Lattn_fill_wait
	s_add_u32 s40, s40, 0x1800
	s_addc_u32 s41, s41, 0
	global_load_dword v95, v2, s[40:41]
	global_load_dword v96, v2, s[40:41] offset:2048
	global_load_dword v97, v3, s[40:41]

.LBB4_63:
	s_endpgm
	s_endpgm
	s_endpgm
	s_endpgm
	s_endpgm
	s_endpgm
	s_endpgm
	s_endpgm
	s_endpgm
	s_endpgm
	s_endpgm
	.section	.rodata,"a",@progbits
	.p2align	6, 0x0

_Z9ln_kernelILi1ELi1EEvPKflS1_S1_S1_S1_S1_S1_S1_PfPDF16_S3_iii:
	s_bitcmp1_b32 s2, 8
	s_cbranch_scc0 .Lprio_skip_q1
	s_setprio 1
.Lprio_skip_q1:
	s_load_dwordx4 s[8:11], s[0:1], 0x38
	s_load_dwordx4 s[16:19], s[0:1], 0x60
	s_load_dwordx2 s[20:21], s[0:1], 0x10
	s_load_dwordx4 s[12:15], s[0:1], 0x20
	v_lshrrev_b32_e32 v1, 6, v0
	v_lshl_or_b32 v2, s2, 2, v1
	s_waitcnt lgkmcnt(0)
	s_cmp_gt_i32 s17, -1
	v_ashrrev_i32_e32 v3, 31, v2
	v_sub_u32_e32 v1, 0, v2
	s_cbranch_scc0 .LBB12_2
	s_abs_i32 s4, s16
	v_cvt_f32_u32_e32 v7, s4
	s_ashr_i32 s2, s18, 31
	v_mov_b32_e32 v4, s18
	v_mov_b32_e32 v5, s2
	v_rcp_iflag_f32_e32 v8, v7
	v_mad_u64_u32 v[4:5], s[2:3], s17, v2, v[4:5]
	v_mov_b32_e32 v6, v5
	v_mad_u64_u32 v[6:7], s[2:3], s17, v3, v[6:7]
	v_mul_f32_e32 v7, 0x4f7ffffe, v8
	v_cvt_u32_f32_e32 v7, v7
	s_sub_i32 s2, 0, s4
	v_max_i32_e32 v8, v2, v1
	v_mov_b32_e32 v5, v6
	v_mul_lo_u32 v9, s2, v7
	v_mul_hi_u32 v9, v7, v9
	v_add_u32_e32 v7, v7, v9
	v_mul_hi_u32 v7, v8, v7
	v_mul_lo_u32 v9, v7, s4
	v_sub_u32_e32 v8, v8, v9
	v_add_u32_e32 v9, 1, v7
	v_cmp_le_u32_e32 vcc, s4, v8
	v_xor_b32_e32 v6, s16, v2
	v_ashrrev_i32_e32 v6, 31, v6
	v_cndmask_b32_e32 v7, v7, v9, vcc
	v_subrev_u32_e32 v9, s4, v8
	v_cndmask_b32_e32 v8, v8, v9, vcc
	v_add_u32_e32 v9, 1, v7
	v_cmp_le_u32_e32 vcc, s4, v8
	s_mov_b64 s[26:27], 0
	s_nop 0
	v_cndmask_b32_e32 v7, v7, v9, vcc
	v_xor_b32_e32 v7, v7, v6
	v_sub_u32_e32 v6, v7, v6
	v_ashrrev_i32_e32 v7, 31, v6
	s_branch .LBB12_3

.LBB12_5:
	v_lshlrev_b32_e32 v0, 2, v0
	v_and_b32_e32 v58, 0xfc, v0
	v_lshlrev_b64 v[4:5], 11, v[4:5]
	v_lshlrev_b32_e32 v0, 2, v58
	v_mov_b32_e32 v1, 0
	s_waitcnt lgkmcnt(0)
	v_lshl_add_u64 v[4:5], s[24:25], 0, v[4:5]
	v_lshl_add_u64 v[4:5], v[4:5], 0, v[0:1]
	global_load_dwordx4 v[8:11], v[4:5], off
	global_load_dwordx4 v[12:15], v0, s[20:21]
	global_load_dwordx4 v[16:19], v0, s[20:21] offset:1024
	global_load_dwordx4 v[20:23], v[4:5], off offset:1024
	v_lshlrev_b64 v[4:5], 11, v[2:3]
	v_lshl_add_u64 v[24:25], s[22:23], 0, v[4:5]
	v_lshl_add_u64 v[40:41], v[24:25], 0, v[0:1]
	global_load_dwordx4 v[24:27], v[40:41], off
	global_load_dwordx4 v[28:31], v[40:41], off offset:1024
	global_load_dwordx4 v[32:35], v0, s[12:13]
	global_load_dwordx4 v[36:39], v0, s[12:13] offset:1024
	v_lshlrev_b64 v[6:7], 11, v[6:7]
	v_lshl_add_u64 v[6:7], s[18:19], 0, v[6:7]
	v_lshl_add_u64 v[52:53], v[6:7], 0, v[0:1]
	global_load_dwordx4 v[40:43], v0, s[14:15]
	global_load_dwordx4 v[44:47], v0, s[8:9]
	global_load_dwordx4 v[48:51], v0, s[10:11]
	v_mov_b32_e32 v59, 0x3727c5ac
	s_mov_b32 s12, 0xf800000
	v_mov_b32_e32 v60, 0x260
	v_lshl_add_u64 v[4:5], s[4:5], 0, v[4:5]
	v_lshlrev_b64 v[2:3], 10, v[2:3]
	s_waitcnt vmcnt(9)
	v_pk_add_f32 v[54:55], v[12:13], v[8:9]
	global_load_dwordx4 v[6:9], v0, s[14:15] offset:1024
	s_waitcnt vmcnt(8)
	v_pk_add_f32 v[20:21], v[16:17], v[20:21]
	v_pk_add_f32 v[18:19], v[18:19], v[22:23]
	v_pk_add_f32 v[56:57], v[14:15], v[10:11]
	global_load_dwordx4 v[10:13], v0, s[8:9] offset:1024
	global_load_dwordx4 v[14:17], v0, s[10:11] offset:1024
	s_waitcnt vmcnt(9)
	v_pk_add_f32 v[54:55], v[24:25], v[54:55]
	s_waitcnt vmcnt(8)
	v_pk_add_f32 v[28:29], v[28:29], v[20:21]
	v_pk_add_f32 v[30:31], v[30:31], v[18:19]
	global_load_dwordx4 v[18:21], v[52:53], off
	global_load_dwordx4 v[22:25], v[52:53], off offset:1024
	v_add_f32_e32 v52, 0, v54
	v_pk_add_f32 v[26:27], v[26:27], v[56:57]
	v_add_f32_e32 v52, v52, v55
	v_add_f32_e32 v52, v52, v26
	v_add_f32_e32 v52, v52, v27
	v_add_f32_e32 v52, v52, v28
	v_add_f32_e32 v52, v52, v29
	v_add_f32_e32 v52, v52, v30
	v_add_f32_e32 v52, v52, v31
	s_nop 1
	v_add_f32_dpp v52, v52, v52 quad_perm:[1,0,3,2] row_mask:0xf bank_mask:0xf bound_ctrl:1
	s_nop 1
	v_add_f32_dpp v52, v52, v52 quad_perm:[2,3,0,1] row_mask:0xf bank_mask:0xf bound_ctrl:1
	s_nop 1
	v_add_f32_dpp v52, v52, v52 row_half_mirror row_mask:0xf bank_mask:0xf bound_ctrl:1
	s_nop 1
	v_add_f32_dpp v52, v52, v52 row_mirror row_mask:0xf bank_mask:0xf bound_ctrl:1
	s_nop 0
	v_readlane_b32 s8, v52, 16
	v_readlane_b32 s9, v52, 48
	v_readlane_b32 s0, v52, 0
	v_readlane_b32 s1, v52, 32
	v_mov_b32_e32 v52, s8
	v_mov_b32_e32 v53, s9
	v_pk_add_f32 v[52:53], s[0:1], v[52:53]
	s_nop 0
	v_add_f32_e32 v52, v52, v53
	v_mul_f32_e32 v52, 0x3b000000, v52
	v_pk_add_f32 v[54:55], v[54:55], v[52:53] op_sel_hi:[1,0] neg_lo:[0,1] neg_hi:[0,1]
	v_pk_add_f32 v[26:27], v[26:27], v[52:53] op_sel_hi:[1,0] neg_lo:[0,1] neg_hi:[0,1]
	v_pk_add_f32 v[28:29], v[28:29], v[52:53] op_sel_hi:[1,0] neg_lo:[0,1] neg_hi:[0,1]
	v_pk_add_f32 v[30:31], v[30:31], v[52:53] op_sel_hi:[1,0] neg_lo:[0,1] neg_hi:[0,1]
	v_pk_mul_f32 v[52:53], v[54:55], v[54:55]
	s_waitcnt vmcnt(9)
	v_pk_mul_f32 v[32:33], v[32:33], v[54:55]
	v_add_f32_e32 v56, v52, v53
	v_pk_mul_f32 v[52:53], v[26:27], v[26:27]
	v_pk_mul_f32 v[26:27], v[34:35], v[26:27]
	v_add_f32_e32 v52, v56, v52
	v_add_f32_e32 v56, v52, v53
	v_pk_mul_f32 v[52:53], v[28:29], v[28:29]
	s_waitcnt vmcnt(8)
	v_pk_mul_f32 v[28:29], v[36:37], v[28:29]
	v_add_f32_e32 v52, v56, v52
	v_add_f32_e32 v56, v52, v53
	v_pk_mul_f32 v[52:53], v[30:31], v[30:31]
	v_pk_mul_f32 v[30:31], v[38:39], v[30:31]
	v_add_f32_e32 v52, v56, v52
	v_add_f32_e32 v52, v52, v53
	s_nop 1
	v_add_f32_dpp v52, v52, v52 quad_perm:[1,0,3,2] row_mask:0xf bank_mask:0xf bound_ctrl:1
	s_nop 1
	v_add_f32_dpp v52, v52, v52 quad_perm:[2,3,0,1] row_mask:0xf bank_mask:0xf bound_ctrl:1
	s_nop 1
	v_add_f32_dpp v52, v52, v52 row_half_mirror row_mask:0xf bank_mask:0xf bound_ctrl:1
	s_nop 1
	v_add_f32_dpp v52, v52, v52 row_mirror row_mask:0xf bank_mask:0xf bound_ctrl:1
	s_nop 0
	v_readlane_b32 s8, v52, 16
	v_readlane_b32 s9, v52, 48
	v_readlane_b32 s0, v52, 0
	v_readlane_b32 s1, v52, 32
	v_mov_b32_e32 v52, s8
	v_mov_b32_e32 v53, s9
	v_pk_add_f32 v[52:53], s[0:1], v[52:53]
	s_nop 0
	v_add_f32_e32 v52, v52, v53
	v_fmamk_f32 v52, v52, 0x3b000000, v59
	v_mul_f32_e32 v53, 0x4f800000, v52
	v_cmp_gt_f32_e32 vcc, s12, v52
	s_nop 1
	v_cndmask_b32_e32 v52, v52, v53, vcc
	v_sqrt_f32_e32 v53, v52
	s_nop 0
	v_add_u32_e32 v34, -1, v53
	v_add_u32_e32 v35, 1, v53
	v_fma_f32 v36, -v34, v53, v52
	v_fma_f32 v37, -v35, v53, v52
	v_cmp_ge_f32_e64 s[0:1], 0, v36
	s_nop 1
	v_cndmask_b32_e64 v34, v53, v34, s[0:1]
	v_cmp_lt_f32_e64 s[0:1], 0, v37
	s_nop 1
	v_cndmask_b32_e64 v34, v34, v35, s[0:1]
	v_mul_f32_e32 v35, 0x37800000, v34
	v_cndmask_b32_e32 v34, v34, v35, vcc
	v_cmp_class_f32_e32 vcc, v52, v60
	s_nop 1
	v_cndmask_b32_e32 v34, v34, v52, vcc
	v_div_scale_f32 v35, s[0:1], v34, v34, 1.0
	v_rcp_f32_e32 v36, v35
	v_div_scale_f32 v37, vcc, 1.0, v34, 1.0
	v_fma_f32 v38, -v35, v36, 1.0
	v_fmac_f32_e32 v36, v38, v36
	v_mul_f32_e32 v38, v37, v36
	v_fma_f32 v39, -v35, v38, v37
	v_fmac_f32_e32 v38, v39, v36
	v_fma_f32 v35, -v35, v38, v37
	v_div_fmas_f32 v35, v35, v36, v38
	v_div_fixup_f32 v34, v35, v34, 1.0
	s_waitcnt vmcnt(7)
	v_pk_fma_f32 v[32:33], v[34:35], v[32:33], v[40:41] op_sel_hi:[0,1,1]
	s_waitcnt vmcnt(4)
	v_pk_fma_f32 v[6:7], v[34:35], v[28:29], v[6:7] op_sel_hi:[0,1,1]
	s_waitcnt vmcnt(1)
	v_pk_add_f32 v[18:19], v[32:33], v[18:19]
	v_pk_fma_f32 v[26:27], v[34:35], v[26:27], v[42:43] op_sel_hi:[0,1,1]
	s_waitcnt vmcnt(0)
	v_pk_add_f32 v[6:7], v[6:7], v[22:23]
	v_add_f32_e32 v22, 0, v18
	v_pk_add_f32 v[20:21], v[26:27], v[20:21]
	v_add_f32_e32 v22, v22, v19
	v_add_f32_e32 v22, v22, v20
	v_add_f32_e32 v22, v22, v21
	v_pk_fma_f32 v[8:9], v[34:35], v[30:31], v[8:9] op_sel_hi:[0,1,1]
	v_add_f32_e32 v22, v22, v6
	v_pk_add_f32 v[8:9], v[8:9], v[24:25]
	v_add_f32_e32 v22, v22, v7
	v_add_f32_e32 v22, v22, v8
	v_add_f32_e32 v22, v22, v9
	s_nop 1
	v_add_f32_dpp v22, v22, v22 quad_perm:[1,0,3,2] row_mask:0xf bank_mask:0xf bound_ctrl:1
	s_nop 1
	v_add_f32_dpp v22, v22, v22 quad_perm:[2,3,0,1] row_mask:0xf bank_mask:0xf bound_ctrl:1
	s_nop 1
	v_add_f32_dpp v22, v22, v22 row_half_mirror row_mask:0xf bank_mask:0xf bound_ctrl:1
	s_nop 1
	v_add_f32_dpp v22, v22, v22 row_mirror row_mask:0xf bank_mask:0xf bound_ctrl:1
	s_nop 0
	v_readlane_b32 s8, v22, 16
	v_readlane_b32 s9, v22, 48
	v_readlane_b32 s0, v22, 0
	v_readlane_b32 s1, v22, 32
	v_mov_b32_e32 v22, s8
	v_mov_b32_e32 v23, s9
	v_pk_add_f32 v[22:23], s[0:1], v[22:23]
	s_nop 0
	v_add_f32_e32 v22, v22, v23
	v_mul_f32_e32 v22, 0x3b000000, v22
	v_pk_add_f32 v[18:19], v[18:19], v[22:23] op_sel_hi:[1,0] neg_lo:[0,1] neg_hi:[0,1]
	v_pk_add_f32 v[20:21], v[20:21], v[22:23] op_sel_hi:[1,0] neg_lo:[0,1] neg_hi:[0,1]
	v_pk_add_f32 v[24:25], v[6:7], v[22:23] op_sel_hi:[1,0] neg_lo:[0,1] neg_hi:[0,1]
	v_pk_mul_f32 v[6:7], v[18:19], v[18:19]
	v_pk_add_f32 v[22:23], v[8:9], v[22:23] op_sel_hi:[1,0] neg_lo:[0,1] neg_hi:[0,1]
	v_pk_mul_f32 v[8:9], v[20:21], v[20:21]
	v_add_f32_e32 v6, v6, v7
	v_add_f32_e32 v6, v6, v8
	v_pk_mul_f32 v[26:27], v[24:25], v[24:25]
	v_add_f32_e32 v6, v6, v9
	v_add_f32_e32 v6, v6, v26
	v_pk_mul_f32 v[28:29], v[22:23], v[22:23]
	v_add_f32_e32 v6, v6, v27
	v_add_f32_e32 v6, v6, v28
	v_add_f32_e32 v6, v6, v29
	s_nop 1
	v_add_f32_dpp v6, v6, v6 quad_perm:[1,0,3,2] row_mask:0xf bank_mask:0xf bound_ctrl:1
	s_nop 1
	v_add_f32_dpp v6, v6, v6 quad_perm:[2,3,0,1] row_mask:0xf bank_mask:0xf bound_ctrl:1
	s_nop 1
	v_add_f32_dpp v6, v6, v6 row_half_mirror row_mask:0xf bank_mask:0xf bound_ctrl:1
	s_nop 1
	v_add_f32_dpp v6, v6, v6 row_mirror row_mask:0xf bank_mask:0xf bound_ctrl:1
	s_nop 0
	v_readlane_b32 s8, v6, 16
	v_readlane_b32 s9, v6, 48
	v_readlane_b32 s0, v6, 0
	v_readlane_b32 s1, v6, 32
	v_mov_b32_e32 v6, s8
	v_mov_b32_e32 v7, s9
	v_pk_add_f32 v[6:7], s[0:1], v[6:7]
	s_nop 0
	v_add_f32_e32 v6, v6, v7
	v_fmac_f32_e32 v59, 0x3b000000, v6
	v_mul_f32_e32 v6, 0x4f800000, v59
	v_cmp_gt_f32_e32 vcc, s12, v59
	s_nop 1
	v_cndmask_b32_e32 v6, v59, v6, vcc
	v_sqrt_f32_e32 v7, v6
	s_nop 0
	v_add_u32_e32 v8, -1, v7
	v_add_u32_e32 v9, 1, v7
	v_fma_f32 v26, -v8, v7, v6
	v_fma_f32 v27, -v9, v7, v6
	v_cmp_ge_f32_e64 s[0:1], 0, v26
	s_nop 1
	v_cndmask_b32_e64 v7, v7, v8, s[0:1]
	v_cmp_lt_f32_e64 s[0:1], 0, v27
	v_lshl_add_u64 v[26:27], v[4:5], 0, v[0:1]
	s_nop 0
	v_cndmask_b32_e64 v7, v7, v9, s[0:1]
	v_mul_f32_e32 v8, 0x37800000, v7
	v_cndmask_b32_e32 v7, v7, v8, vcc
	v_cmp_class_f32_e32 vcc, v6, v60
	s_nop 1
	v_cndmask_b32_e32 v6, v7, v6, vcc
	v_div_scale_f32 v7, s[0:1], v6, v6, 1.0
	v_rcp_f32_e32 v8, v7
	s_mov_b32 s0, 0x43000000
	v_fma_f32 v0, -v7, v8, 1.0
	v_fmac_f32_e32 v8, v0, v8
	v_div_scale_f32 v0, vcc, 1.0, v6, 1.0
	v_mul_f32_e32 v4, v0, v8
	v_fma_f32 v5, -v7, v4, v0
	v_fmac_f32_e32 v4, v5, v8
	v_fma_f32 v0, -v7, v4, v0
	v_div_fmas_f32 v0, v0, v8, v4
	v_div_fixup_f32 v0, v0, v6, 1.0
	v_pk_mul_f32 v[4:5], v[44:45], v[18:19]
	v_pk_mul_f32 v[6:7], v[46:47], v[20:21]
	v_pk_fma_f32 v[4:5], v[0:1], v[4:5], v[48:49] op_sel_hi:[0,1,1]
	v_pk_mul_f32 v[8:9], v[10:11], v[24:25]
	v_pk_fma_f32 v[6:7], v[0:1], v[6:7], v[50:51] op_sel_hi:[0,1,1]
	v_pk_fma_f32 v[8:9], v[0:1], v[8:9], v[14:15] op_sel_hi:[0,1,1]
	v_pk_mul_f32 v[10:11], v[12:13], v[22:23]
	v_fma_mixlo_f16 v12, v4, s0, 0
	v_pk_fma_f32 v[10:11], v[0:1], v[10:11], v[16:17] op_sel_hi:[0,1,1]
	global_store_dwordx4 v[26:27], v[4:7], off sc1
	global_store_dwordx4 v[26:27], v[8:11], off offset:1024 sc1
	v_mul_f32_e32 v0, 0x43000000, v4
	v_fma_mixlo_f16 v4, v4, s0, -v12 op_sel_hi:[0,0,1]
	v_fma_mixlo_f16 v12, v8, s0, 0
	v_mul_f32_e32 v13, 0x43000000, v8
	v_fma_mixlo_f16 v8, v8, s0, -v12 op_sel_hi:[0,0,1]
	v_mul_f32_e32 v12, 0x43000000, v5
	v_fma_mixlo_f16 v14, v5, s0, 0
	v_cvt_pk_f16_f32 v12, v0, v12
	v_mul_f32_e32 v0, 0x43000000, v9
	v_pk_mul_f32 v[16:17], v[6:7], s[0:1] op_sel_hi:[1,0]
	v_fma_mixhi_f16 v4, v5, s0, -v14 op_sel_hi:[0,0,1]
	v_cvt_pk_f16_f32 v14, v13, v0
	v_cvt_pk_f16_f32 v13, v16, v17
	v_pk_mul_f32 v[18:19], v[10:11], s[0:1] op_sel_hi:[1,0]
	v_cvt_f32_f16_e32 v16, v13
	v_cvt_f32_f16_sdwa v17, v13 dst_sel:DWORD dst_unused:UNUSED_PAD src0_sel:WORD_1
	v_cvt_pk_f16_f32 v15, v18, v19
	v_cvt_f32_f16_e32 v18, v15
	v_cvt_f32_f16_sdwa v19, v15 dst_sel:DWORD dst_unused:UNUSED_PAD src0_sel:WORD_1
	v_fma_mixlo_f16 v5, v9, s0, 0
	v_pk_fma_f32 v[6:7], v[6:7], s[0:1], v[16:17] op_sel_hi:[1,0,1] neg_lo:[0,0,1] neg_hi:[0,0,1]
	v_fma_mixhi_f16 v8, v9, s0, -v5 op_sel_hi:[0,0,1]
	v_cvt_pk_f16_f32 v5, v6, v7
	v_pk_fma_f32 v[6:7], v[10:11], s[0:1], v[18:19] op_sel_hi:[1,0,1] neg_lo:[0,0,1] neg_hi:[0,0,1]
	v_lshlrev_b32_e32 v0, 1, v58
	v_cvt_pk_f16_f32 v9, v6, v7
	v_lshl_add_u64 v[6:7], s[6:7], 0, v[2:3]
	v_lshl_add_u64 v[2:3], s[2:3], 0, v[2:3]
	v_lshl_add_u64 v[6:7], v[6:7], 0, v[0:1]
	v_lshl_add_u64 v[0:1], v[2:3], 0, v[0:1]
	global_store_dwordx2 v[6:7], v[12:13], off
	global_store_dwordx2 v[6:7], v[14:15], off offset:512
	global_store_dwordx2 v[0:1], v[4:5], off
	global_store_dwordx2 v[0:1], v[8:9], off offset:512
	s_endpgm
	s_endpgm
	s_endpgm
	s_endpgm
	s_endpgm
	s_endpgm
	s_endpgm
	s_endpgm
	s_endpgm
	s_endpgm
	s_endpgm
	s_endpgm
	s_endpgm
	s_endpgm
	s_endpgm
	s_endpgm
	s_endpgm
	s_endpgm
	s_endpgm
	s_endpgm
	s_endpgm
	s_endpgm
	s_endpgm
	s_endpgm
	s_endpgm
	s_endpgm
	s_endpgm
	s_endpgm
	s_endpgm
	s_endpgm
	s_endpgm
	s_endpgm
	s_endpgm
	s_endpgm
	s_endpgm
	s_endpgm
	s_endpgm
	s_endpgm
	s_endpgm
	s_endpgm
	s_endpgm
	s_endpgm
	s_endpgm
	s_endpgm
	s_endpgm
	s_endpgm
	.section	.rodata,"a",@progbits
	.p2align	6, 0x0

_Z9ln_kernelILi1ELi2EEvPKflS1_S1_S1_S1_S1_S1_S1_PfPDF16_S3_iii:
	s_bitcmp1_b32 s2, 8
	s_cbranch_scc0 .Lprio_skip_q2
	s_setprio 1

.LBB13_5:
	v_lshlrev_b32_e32 v0, 2, v0
	v_and_b32_e32 v58, 0xfc, v0
	v_lshlrev_b64 v[4:5], 11, v[4:5]
	s_load_dwordx2 s[0:1], s[0:1], 0x8
	v_lshlrev_b32_e32 v0, 2, v58
	v_mov_b32_e32 v1, 0
	s_waitcnt lgkmcnt(0)
	v_lshl_add_u64 v[4:5], s[24:25], 0, v[4:5]
	v_lshl_add_u64 v[4:5], v[4:5], 0, v[0:1]
	global_load_dwordx4 v[8:11], v[4:5], off
	global_load_dwordx4 v[12:15], v0, s[20:21]
	global_load_dwordx4 v[16:19], v0, s[20:21] offset:1024
	global_load_dwordx4 v[20:23], v[4:5], off offset:1024
	v_lshlrev_b64 v[4:5], 11, v[2:3]
	v_lshl_add_u64 v[32:33], s[22:23], 0, v[4:5]
	v_lshl_add_u64 v[34:35], v[32:33], 0, v[0:1]
	v_lshl_add_u64 v[32:33], s[0:1], 2, v[32:33]
	global_load_dwordx4 v[24:27], v[34:35], off
	global_load_dwordx4 v[28:31], v[34:35], off offset:1024
	v_lshl_add_u64 v[40:41], v[32:33], 0, v[0:1]
	global_load_dwordx4 v[32:35], v[40:41], off
	global_load_dwordx4 v[36:39], v[40:41], off offset:1024
	global_load_dwordx4 v[44:47], v0, s[12:13] offset:1024
	v_lshlrev_b64 v[6:7], 11, v[6:7]
	global_load_dwordx4 v[40:43], v0, s[12:13]
	v_lshl_add_u64 v[6:7], s[18:19], 0, v[6:7]
	global_load_dwordx4 v[48:51], v0, s[14:15]
	v_lshl_add_u64 v[52:53], v[6:7], 0, v[0:1]
	v_mov_b32_e32 v59, 0x3727c5ac
	s_mov_b32 s12, 0xf800000
	v_mov_b32_e32 v60, 0x260
	v_lshl_add_u64 v[4:5], s[4:5], 0, v[4:5]
	v_lshlrev_b64 v[2:3], 10, v[2:3]
	s_waitcnt vmcnt(9)
	v_pk_add_f32 v[54:55], v[12:13], v[8:9]
	v_pk_add_f32 v[56:57], v[14:15], v[10:11]
	s_waitcnt vmcnt(7)
	v_pk_add_f32 v[20:21], v[16:17], v[20:21]
	v_pk_add_f32 v[18:19], v[18:19], v[22:23]
	global_load_dwordx4 v[6:9], v0, s[8:9]
	global_load_dwordx4 v[10:13], v0, s[10:11]
	global_load_dwordx4 v[14:17], v0, s[14:15] offset:1024
	s_waitcnt vmcnt(9)
	v_pk_add_f32 v[54:55], v[54:55], v[24:25]
	v_pk_add_f32 v[26:27], v[56:57], v[26:27]
	s_waitcnt vmcnt(8)
	v_pk_add_f32 v[28:29], v[20:21], v[28:29]
	v_pk_add_f32 v[30:31], v[18:19], v[30:31]
	global_load_dwordx4 v[18:21], v0, s[8:9] offset:1024
	global_load_dwordx4 v[22:25], v0, s[10:11] offset:1024
	s_waitcnt vmcnt(9)
	v_pk_add_f32 v[54:55], v[54:55], v[32:33]
	v_pk_add_f32 v[34:35], v[26:27], v[34:35]
	s_waitcnt vmcnt(8)
	v_pk_add_f32 v[36:37], v[28:29], v[36:37]
	v_pk_add_f32 v[38:39], v[30:31], v[38:39]
	global_load_dwordx4 v[26:29], v[52:53], off
	global_load_dwordx4 v[30:33], v[52:53], off offset:1024
	v_add_f32_e32 v52, 0, v54
	v_add_f32_e32 v52, v52, v55
	v_add_f32_e32 v52, v52, v34
	v_add_f32_e32 v52, v52, v35
	v_add_f32_e32 v52, v52, v36
	v_add_f32_e32 v52, v52, v37
	v_add_f32_e32 v52, v52, v38
	v_add_f32_e32 v52, v52, v39
	s_nop 1
	v_add_f32_dpp v52, v52, v52 quad_perm:[1,0,3,2] row_mask:0xf bank_mask:0xf bound_ctrl:1
	s_nop 1
	v_add_f32_dpp v52, v52, v52 quad_perm:[2,3,0,1] row_mask:0xf bank_mask:0xf bound_ctrl:1
	s_nop 1
	v_add_f32_dpp v52, v52, v52 row_half_mirror row_mask:0xf bank_mask:0xf bound_ctrl:1
	s_nop 1
	v_add_f32_dpp v52, v52, v52 row_mirror row_mask:0xf bank_mask:0xf bound_ctrl:1
	s_nop 0
	v_readlane_b32 s8, v52, 16
	v_readlane_b32 s9, v52, 48
	v_readlane_b32 s0, v52, 0
	v_readlane_b32 s1, v52, 32
	v_mov_b32_e32 v52, s8
	v_mov_b32_e32 v53, s9
	v_pk_add_f32 v[52:53], s[0:1], v[52:53]
	s_nop 0
	v_add_f32_e32 v52, v52, v53
	v_mul_f32_e32 v52, 0x3b000000, v52
	v_pk_add_f32 v[54:55], v[54:55], v[52:53] op_sel_hi:[1,0] neg_lo:[0,1] neg_hi:[0,1]
	v_pk_add_f32 v[34:35], v[34:35], v[52:53] op_sel_hi:[1,0] neg_lo:[0,1] neg_hi:[0,1]
	v_pk_add_f32 v[36:37], v[36:37], v[52:53] op_sel_hi:[1,0] neg_lo:[0,1] neg_hi:[0,1]
	v_pk_add_f32 v[38:39], v[38:39], v[52:53] op_sel_hi:[1,0] neg_lo:[0,1] neg_hi:[0,1]
	v_pk_mul_f32 v[52:53], v[54:55], v[54:55]
	s_waitcnt vmcnt(8)
	v_pk_mul_f32 v[40:41], v[40:41], v[54:55]
	v_add_f32_e32 v56, v52, v53
	v_pk_mul_f32 v[52:53], v[34:35], v[34:35]
	v_pk_mul_f32 v[34:35], v[42:43], v[34:35]
	v_add_f32_e32 v52, v56, v52
	v_add_f32_e32 v56, v52, v53
	v_pk_mul_f32 v[52:53], v[36:37], v[36:37]
	v_pk_mul_f32 v[36:37], v[44:45], v[36:37]
	v_add_f32_e32 v52, v56, v52
	v_add_f32_e32 v56, v52, v53
	v_pk_mul_f32 v[52:53], v[38:39], v[38:39]
	v_pk_mul_f32 v[38:39], v[46:47], v[38:39]
	v_add_f32_e32 v52, v56, v52
	v_add_f32_e32 v52, v52, v53
	s_nop 1
	v_add_f32_dpp v52, v52, v52 quad_perm:[1,0,3,2] row_mask:0xf bank_mask:0xf bound_ctrl:1
	s_nop 1
	v_add_f32_dpp v52, v52, v52 quad_perm:[2,3,0,1] row_mask:0xf bank_mask:0xf bound_ctrl:1
	s_nop 1
	v_add_f32_dpp v52, v52, v52 row_half_mirror row_mask:0xf bank_mask:0xf bound_ctrl:1
	s_nop 1
	v_add_f32_dpp v52, v52, v52 row_mirror row_mask:0xf bank_mask:0xf bound_ctrl:1
	s_nop 0
	v_readlane_b32 s8, v52, 16
	v_readlane_b32 s9, v52, 48
	v_readlane_b32 s0, v52, 0
	v_readlane_b32 s1, v52, 32
	v_mov_b32_e32 v52, s8
	v_mov_b32_e32 v53, s9
	v_pk_add_f32 v[52:53], s[0:1], v[52:53]
	s_nop 0
	v_add_f32_e32 v52, v52, v53
	v_fmamk_f32 v52, v52, 0x3b000000, v59
	v_mul_f32_e32 v53, 0x4f800000, v52
	v_cmp_gt_f32_e32 vcc, s12, v52
	s_nop 1
	v_cndmask_b32_e32 v52, v52, v53, vcc
	v_sqrt_f32_e32 v53, v52
	s_nop 0
	v_add_u32_e32 v42, -1, v53
	v_add_u32_e32 v43, 1, v53
	v_fma_f32 v44, -v42, v53, v52
	v_fma_f32 v45, -v43, v53, v52
	v_cmp_ge_f32_e64 s[0:1], 0, v44
	s_nop 1
	v_cndmask_b32_e64 v42, v53, v42, s[0:1]
	v_cmp_lt_f32_e64 s[0:1], 0, v45
	s_nop 1
	v_cndmask_b32_e64 v42, v42, v43, s[0:1]
	v_mul_f32_e32 v43, 0x37800000, v42
	v_cndmask_b32_e32 v42, v42, v43, vcc
	v_cmp_class_f32_e32 vcc, v52, v60
	s_nop 1
	v_cndmask_b32_e32 v42, v42, v52, vcc
	v_div_scale_f32 v43, s[0:1], v42, v42, 1.0
	v_rcp_f32_e32 v44, v43
	v_div_scale_f32 v45, vcc, 1.0, v42, 1.0
	v_fma_f32 v46, -v43, v44, 1.0
	v_fmac_f32_e32 v44, v46, v44
	v_mul_f32_e32 v46, v45, v44
	v_fma_f32 v47, -v43, v46, v45
	v_fmac_f32_e32 v46, v47, v44
	v_fma_f32 v43, -v43, v46, v45
	v_div_fmas_f32 v43, v43, v44, v46
	v_div_fixup_f32 v42, v43, v42, 1.0
	s_waitcnt vmcnt(7)
	v_pk_fma_f32 v[40:41], v[42:43], v[40:41], v[48:49] op_sel_hi:[0,1,1]
	s_waitcnt vmcnt(4)
	v_pk_fma_f32 v[14:15], v[42:43], v[36:37], v[14:15] op_sel_hi:[0,1,1]
	s_waitcnt vmcnt(1)
	v_pk_add_f32 v[26:27], v[40:41], v[26:27]
	v_pk_fma_f32 v[34:35], v[42:43], v[34:35], v[50:51] op_sel_hi:[0,1,1]
	s_waitcnt vmcnt(0)
	v_pk_add_f32 v[14:15], v[14:15], v[30:31]
	v_add_f32_e32 v30, 0, v26
	v_pk_add_f32 v[28:29], v[34:35], v[28:29]
	v_add_f32_e32 v30, v30, v27
	v_add_f32_e32 v30, v30, v28
	v_add_f32_e32 v30, v30, v29
	v_pk_fma_f32 v[16:17], v[42:43], v[38:39], v[16:17] op_sel_hi:[0,1,1]
	v_add_f32_e32 v30, v30, v14
	v_pk_add_f32 v[16:17], v[16:17], v[32:33]
	v_add_f32_e32 v30, v30, v15
	v_add_f32_e32 v30, v30, v16
	v_add_f32_e32 v30, v30, v17
	s_nop 1
	v_add_f32_dpp v30, v30, v30 quad_perm:[1,0,3,2] row_mask:0xf bank_mask:0xf bound_ctrl:1
	s_nop 1
	v_add_f32_dpp v30, v30, v30 quad_perm:[2,3,0,1] row_mask:0xf bank_mask:0xf bound_ctrl:1
	s_nop 1
	v_add_f32_dpp v30, v30, v30 row_half_mirror row_mask:0xf bank_mask:0xf bound_ctrl:1
	s_nop 1
	v_add_f32_dpp v30, v30, v30 row_mirror row_mask:0xf bank_mask:0xf bound_ctrl:1
	s_nop 0
	v_readlane_b32 s8, v30, 16
	v_readlane_b32 s9, v30, 48
	v_readlane_b32 s0, v30, 0
	v_readlane_b32 s1, v30, 32
	v_mov_b32_e32 v30, s8
	v_mov_b32_e32 v31, s9
	v_pk_add_f32 v[30:31], s[0:1], v[30:31]
	s_nop 0
	v_add_f32_e32 v30, v30, v31
	v_mul_f32_e32 v30, 0x3b000000, v30
	v_pk_add_f32 v[26:27], v[26:27], v[30:31] op_sel_hi:[1,0] neg_lo:[0,1] neg_hi:[0,1]
	v_pk_add_f32 v[28:29], v[28:29], v[30:31] op_sel_hi:[1,0] neg_lo:[0,1] neg_hi:[0,1]
	v_pk_add_f32 v[14:15], v[14:15], v[30:31] op_sel_hi:[1,0] neg_lo:[0,1] neg_hi:[0,1]
	v_pk_add_f32 v[16:17], v[16:17], v[30:31] op_sel_hi:[1,0] neg_lo:[0,1] neg_hi:[0,1]
	v_pk_mul_f32 v[30:31], v[26:27], v[26:27]
	v_pk_mul_f32 v[32:33], v[28:29], v[28:29]
	v_add_f32_e32 v30, v30, v31
	v_add_f32_e32 v30, v30, v32
	v_pk_mul_f32 v[34:35], v[14:15], v[14:15]
	v_add_f32_e32 v30, v30, v33
	v_add_f32_e32 v30, v30, v34
	v_pk_mul_f32 v[36:37], v[16:17], v[16:17]
	v_add_f32_e32 v30, v30, v35
	v_add_f32_e32 v30, v30, v36
	v_add_f32_e32 v30, v30, v37
	s_nop 1
	v_add_f32_dpp v30, v30, v30 quad_perm:[1,0,3,2] row_mask:0xf bank_mask:0xf bound_ctrl:1
	s_nop 1
	v_add_f32_dpp v30, v30, v30 quad_perm:[2,3,0,1] row_mask:0xf bank_mask:0xf bound_ctrl:1
	s_nop 1
	v_add_f32_dpp v30, v30, v30 row_half_mirror row_mask:0xf bank_mask:0xf bound_ctrl:1
	s_nop 1
	v_add_f32_dpp v30, v30, v30 row_mirror row_mask:0xf bank_mask:0xf bound_ctrl:1
	s_nop 0
	v_readlane_b32 s8, v30, 16
	v_readlane_b32 s9, v30, 48
	v_readlane_b32 s0, v30, 0
	v_readlane_b32 s1, v30, 32
	v_mov_b32_e32 v30, s8
	v_mov_b32_e32 v31, s9
	v_pk_add_f32 v[30:31], s[0:1], v[30:31]
	s_nop 0
	v_add_f32_e32 v30, v30, v31
	v_fmac_f32_e32 v59, 0x3b000000, v30
	v_mul_f32_e32 v30, 0x4f800000, v59
	v_cmp_gt_f32_e32 vcc, s12, v59
	s_nop 1
	v_cndmask_b32_e32 v30, v59, v30, vcc
	v_sqrt_f32_e32 v31, v30
	s_nop 0
	v_add_u32_e32 v32, -1, v31
	v_fma_f32 v33, -v32, v31, v30
	v_cmp_ge_f32_e64 s[0:1], 0, v33
	v_add_u32_e32 v33, 1, v31
	s_nop 0
	v_cndmask_b32_e64 v32, v31, v32, s[0:1]
	v_fma_f32 v31, -v33, v31, v30
	v_cmp_lt_f32_e64 s[0:1], 0, v31
	s_nop 1
	v_cndmask_b32_e64 v31, v32, v33, s[0:1]
	v_mul_f32_e32 v32, 0x37800000, v31
	v_cndmask_b32_e32 v31, v31, v32, vcc
	v_cmp_class_f32_e32 vcc, v30, v60
	s_nop 1
	v_cndmask_b32_e32 v32, v31, v30, vcc
	v_div_scale_f32 v33, s[0:1], v32, v32, 1.0
	v_rcp_f32_e32 v34, v33
	v_lshl_add_u64 v[30:31], v[4:5], 0, v[0:1]
	s_mov_b32 s0, 0x43000000
	v_fma_f32 v0, -v33, v34, 1.0
	v_fmac_f32_e32 v34, v0, v34
	v_div_scale_f32 v0, vcc, 1.0, v32, 1.0
	v_mul_f32_e32 v4, v0, v34
	v_fma_f32 v5, -v33, v4, v0
	v_fmac_f32_e32 v4, v5, v34
	v_fma_f32 v0, -v33, v4, v0
	v_div_fmas_f32 v0, v0, v34, v4
	v_div_fixup_f32 v0, v0, v32, 1.0
	v_pk_mul_f32 v[4:5], v[6:7], v[26:27]
	v_pk_mul_f32 v[6:7], v[8:9], v[28:29]
	v_pk_fma_f32 v[4:5], v[0:1], v[4:5], v[10:11] op_sel_hi:[0,1,1]
	v_pk_mul_f32 v[8:9], v[18:19], v[14:15]
	v_pk_fma_f32 v[6:7], v[0:1], v[6:7], v[12:13] op_sel_hi:[0,1,1]
	v_pk_fma_f32 v[8:9], v[0:1], v[8:9], v[22:23] op_sel_hi:[0,1,1]
	v_pk_mul_f32 v[10:11], v[20:21], v[16:17]
	v_fma_mixlo_f16 v12, v4, s0, 0
	v_pk_fma_f32 v[10:11], v[0:1], v[10:11], v[24:25] op_sel_hi:[0,1,1]
	global_store_dwordx4 v[30:31], v[4:7], off sc1
	global_store_dwordx4 v[30:31], v[8:11], off offset:1024 sc1
	v_mul_f32_e32 v0, 0x43000000, v4
	v_fma_mixlo_f16 v4, v4, s0, -v12 op_sel_hi:[0,0,1]
	v_fma_mixlo_f16 v12, v8, s0, 0
	v_mul_f32_e32 v13, 0x43000000, v8
	v_fma_mixlo_f16 v8, v8, s0, -v12 op_sel_hi:[0,0,1]
	v_mul_f32_e32 v12, 0x43000000, v5
	v_fma_mixlo_f16 v14, v5, s0, 0
	v_cvt_pk_f16_f32 v12, v0, v12
	v_mul_f32_e32 v0, 0x43000000, v9
	v_pk_mul_f32 v[16:17], v[6:7], s[0:1] op_sel_hi:[1,0]
	v_fma_mixhi_f16 v4, v5, s0, -v14 op_sel_hi:[0,0,1]
	v_cvt_pk_f16_f32 v14, v13, v0
	v_cvt_pk_f16_f32 v13, v16, v17
	v_pk_mul_f32 v[18:19], v[10:11], s[0:1] op_sel_hi:[1,0]
	v_cvt_f32_f16_e32 v16, v13
	v_cvt_f32_f16_sdwa v17, v13 dst_sel:DWORD dst_unused:UNUSED_PAD src0_sel:WORD_1
	v_cvt_pk_f16_f32 v15, v18, v19
	v_cvt_f32_f16_e32 v18, v15
	v_cvt_f32_f16_sdwa v19, v15 dst_sel:DWORD dst_unused:UNUSED_PAD src0_sel:WORD_1
	v_fma_mixlo_f16 v5, v9, s0, 0
	v_pk_fma_f32 v[6:7], v[6:7], s[0:1], v[16:17] op_sel_hi:[1,0,1] neg_lo:[0,0,1] neg_hi:[0,0,1]
	v_fma_mixhi_f16 v8, v9, s0, -v5 op_sel_hi:[0,0,1]
	v_cvt_pk_f16_f32 v5, v6, v7
	v_pk_fma_f32 v[6:7], v[10:11], s[0:1], v[18:19] op_sel_hi:[1,0,1] neg_lo:[0,0,1] neg_hi:[0,0,1]
	v_lshlrev_b32_e32 v0, 1, v58
	v_cvt_pk_f16_f32 v9, v6, v7
	v_lshl_add_u64 v[6:7], s[6:7], 0, v[2:3]
	v_lshl_add_u64 v[2:3], s[2:3], 0, v[2:3]
	v_lshl_add_u64 v[6:7], v[6:7], 0, v[0:1]
	v_lshl_add_u64 v[0:1], v[2:3], 0, v[0:1]
	global_store_dwordx2 v[6:7], v[12:13], off
	global_store_dwordx2 v[6:7], v[14:15], off offset:512
	global_store_dwordx2 v[0:1], v[4:5], off
	global_store_dwordx2 v[0:1], v[8:9], off offset:512
	s_endpgm
	s_endpgm
	s_endpgm
	s_endpgm
	s_endpgm
	s_endpgm
	s_endpgm
	s_endpgm
	s_endpgm
	s_endpgm
	s_endpgm
	s_endpgm
	s_endpgm
	s_endpgm
	s_endpgm
	s_endpgm
	s_endpgm
	s_endpgm
	s_endpgm
	s_endpgm
	s_endpgm
	s_endpgm
	s_endpgm
	s_endpgm
	s_endpgm
	s_endpgm
	s_endpgm
	.section	.rodata,"a",@progbits
	.p2align	6, 0x0

_Z9ln_kernelILi1ELi4EEvPKflS1_S1_S1_S1_S1_S1_S1_PfPDF16_S3_iii:
	s_bitcmp1_b32 s2, 8
	s_cbranch_scc0 .Lprio_skip_q3
	s_setprio 1
.Lprio_skip_q3:
	s_load_dwordx4 s[8:11], s[0:1], 0x38
	s_load_dwordx4 s[16:19], s[0:1], 0x60
	s_load_dwordx2 s[20:21], s[0:1], 0x10
	s_load_dwordx4 s[12:15], s[0:1], 0x20
	v_lshrrev_b32_e32 v1, 6, v0
	v_lshl_or_b32 v2, s2, 2, v1
	s_waitcnt lgkmcnt(0)
	s_cmp_gt_i32 s17, -1
	v_ashrrev_i32_e32 v3, 31, v2
	v_sub_u32_e32 v1, 0, v2
	s_cbranch_scc0 .LBB14_2
	s_abs_i32 s4, s16
	v_cvt_f32_u32_e32 v6, s4
	s_ashr_i32 s2, s18, 31
	v_mov_b32_e32 v4, s18
	v_mov_b32_e32 v5, s2
	v_rcp_iflag_f32_e32 v6, v6
	v_mad_u64_u32 v[8:9], s[2:3], s17, v2, v[4:5]
	v_mov_b32_e32 v4, v9
	v_mad_u64_u32 v[4:5], s[2:3], s17, v3, v[4:5]
	v_mul_f32_e32 v5, 0x4f7ffffe, v6
	v_cvt_u32_f32_e32 v5, v5
	s_sub_i32 s2, 0, s4
	v_max_i32_e32 v6, v2, v1
	v_mov_b32_e32 v9, v4
	v_mul_lo_u32 v7, s2, v5
	v_mul_hi_u32 v7, v5, v7
	v_add_u32_e32 v5, v5, v7
	v_mul_hi_u32 v5, v6, v5
	v_mul_lo_u32 v7, v5, s4
	v_sub_u32_e32 v6, v6, v7
	v_add_u32_e32 v7, 1, v5
	v_cmp_le_u32_e32 vcc, s4, v6
	v_xor_b32_e32 v4, s16, v2
	v_ashrrev_i32_e32 v4, 31, v4
	v_cndmask_b32_e32 v5, v5, v7, vcc
	v_subrev_u32_e32 v7, s4, v6
	v_cndmask_b32_e32 v6, v6, v7, vcc
	v_add_u32_e32 v7, 1, v5
	v_cmp_le_u32_e32 vcc, s4, v6
	s_mov_b64 s[26:27], 0
	s_nop 0
	v_cndmask_b32_e32 v5, v5, v7, vcc
	v_xor_b32_e32 v5, v5, v4
	v_sub_u32_e32 v6, v5, v4
	v_ashrrev_i32_e32 v7, 31, v6
	s_branch .LBB14_3

.LBB14_5:
	v_lshlrev_b32_e32 v0, 2, v0
	v_and_b32_e32 v60, 0xfc, v0
	v_lshlrev_b64 v[8:9], 11, v[8:9]
	v_lshlrev_b32_e32 v0, 2, v60
	v_mov_b32_e32 v1, 0
	s_waitcnt lgkmcnt(0)
	v_lshl_add_u64 v[8:9], s[24:25], 0, v[8:9]
	v_lshl_add_u64 v[24:25], v[8:9], 0, v[0:1]
	global_load_dwordx4 v[8:11], v[24:25], off
	global_load_dwordx4 v[12:15], v0, s[20:21]
	global_load_dwordx4 v[16:19], v0, s[20:21] offset:1024
	global_load_dwordx4 v[20:23], v[24:25], off offset:1024
	s_load_dwordx2 s[0:1], s[0:1], 0x8
	v_lshlrev_b64 v[4:5], 11, v[2:3]
	v_lshl_add_u64 v[36:37], s[22:23], 0, v[4:5]
	v_lshl_add_u64 v[28:29], v[36:37], 0, v[0:1]
	global_load_dwordx4 v[24:27], v[28:29], off
	s_waitcnt lgkmcnt(0)
	v_lshl_add_u64 v[30:31], s[0:1], 2, v[36:37]
	v_lshl_add_u64 v[38:39], v[30:31], 0, v[0:1]
	v_lshl_add_u64 v[32:33], s[0:1], 3, v[36:37]
	v_lshl_add_u64 v[44:45], v[32:33], 0, v[0:1]
	global_load_dwordx4 v[32:35], v[38:39], off
	v_mad_u64_u32 v[48:49], s[16:17], s0, 12, v[36:37]
	global_load_dwordx4 v[28:31], v[28:29], off offset:1024
	v_mov_b32_e32 v40, v49
	v_mad_u64_u32 v[46:47], s[0:1], s1, 12, v[40:41]
	global_load_dwordx4 v[40:43], v[44:45], off
	v_mov_b32_e32 v49, v46
	v_lshl_add_u64 v[56:57], v[48:49], 0, v[0:1]
	global_load_dwordx4 v[36:39], v[38:39], off offset:1024
	v_lshlrev_b64 v[6:7], 11, v[6:7]
	global_load_dwordx4 v[44:47], v[44:45], off offset:1024
	s_nop 0
	global_load_dwordx4 v[48:51], v[56:57], off
	global_load_dwordx4 v[52:55], v[56:57], off offset:1024
	v_lshl_add_u64 v[6:7], s[18:19], 0, v[6:7]
	v_lshl_add_u64 v[56:57], v[6:7], 0, v[0:1]
	v_mov_b32_e32 v61, 0x3727c5ac
	s_mov_b32 s16, 0xf800000
	v_lshl_add_u64 v[4:5], s[4:5], 0, v[4:5]
	v_lshlrev_b64 v[2:3], 10, v[2:3]
	s_waitcnt vmcnt(10)
	v_pk_add_f32 v[58:59], v[12:13], v[8:9]
	v_pk_add_f32 v[14:15], v[14:15], v[10:11]
	global_load_dwordx4 v[6:9], v0, s[12:13]
	global_load_dwordx4 v[10:13], v0, s[14:15]
	s_waitcnt vmcnt(10)
	v_pk_add_f32 v[16:17], v[16:17], v[20:21]
	v_pk_add_f32 v[18:19], v[18:19], v[22:23]
	s_waitcnt vmcnt(9)
	v_pk_add_f32 v[22:23], v[58:59], v[24:25]
	v_pk_add_f32 v[24:25], v[14:15], v[26:27]
	s_waitcnt vmcnt(8)
	v_pk_add_f32 v[32:33], v[22:23], v[32:33]
	v_pk_add_f32 v[34:35], v[24:25], v[34:35]
	s_waitcnt vmcnt(7)
	v_pk_add_f32 v[58:59], v[16:17], v[28:29]
	v_pk_add_f32 v[30:31], v[18:19], v[30:31]
	global_load_dwordx4 v[14:17], v0, s[12:13] offset:1024
	global_load_dwordx4 v[18:21], v0, s[14:15] offset:1024
	global_load_dwordx4 v[22:25], v[56:57], off
	global_load_dwordx4 v[26:29], v[56:57], off offset:1024
	s_waitcnt vmcnt(10)
	v_pk_add_f32 v[32:33], v[32:33], v[40:41]
	v_pk_add_f32 v[34:35], v[34:35], v[42:43]
	s_waitcnt vmcnt(9)
	v_pk_add_f32 v[30:31], v[30:31], v[38:39]
	v_pk_add_f32 v[36:37], v[58:59], v[36:37]
	s_waitcnt vmcnt(7)
	v_pk_add_f32 v[32:33], v[32:33], v[48:49]
	v_pk_add_f32 v[34:35], v[34:35], v[50:51]
	v_add_f32_e32 v38, 0, v32
	v_add_f32_e32 v38, v38, v33
	v_pk_add_f32 v[36:37], v[36:37], v[44:45]
	v_add_f32_e32 v38, v38, v34
	s_waitcnt vmcnt(6)
	v_pk_add_f32 v[36:37], v[36:37], v[52:53]
	v_add_f32_e32 v38, v38, v35
	v_pk_add_f32 v[30:31], v[30:31], v[46:47]
	v_add_f32_e32 v38, v38, v36
	v_pk_add_f32 v[30:31], v[30:31], v[54:55]
	v_add_f32_e32 v38, v38, v37
	v_add_f32_e32 v38, v38, v30
	v_add_f32_e32 v38, v38, v31
	v_mov_b32_e32 v55, 0x260
	s_nop 0
	v_add_f32_dpp v38, v38, v38 quad_perm:[1,0,3,2] row_mask:0xf bank_mask:0xf bound_ctrl:1
	s_nop 1
	v_add_f32_dpp v38, v38, v38 quad_perm:[2,3,0,1] row_mask:0xf bank_mask:0xf bound_ctrl:1
	s_nop 1
	v_add_f32_dpp v38, v38, v38 row_half_mirror row_mask:0xf bank_mask:0xf bound_ctrl:1
	s_nop 1
	v_add_f32_dpp v38, v38, v38 row_mirror row_mask:0xf bank_mask:0xf bound_ctrl:1
	s_nop 0
	v_readlane_b32 s12, v38, 16
	v_readlane_b32 s13, v38, 48
	v_readlane_b32 s0, v38, 0
	v_readlane_b32 s1, v38, 32
	v_mov_b32_e32 v38, s12
	v_mov_b32_e32 v39, s13
	v_pk_add_f32 v[38:39], s[0:1], v[38:39]
	s_nop 0
	v_add_f32_e32 v38, v38, v39
	v_mul_f32_e32 v38, 0x3b000000, v38
	v_pk_add_f32 v[46:47], v[32:33], v[38:39] op_sel_hi:[1,0] neg_lo:[0,1] neg_hi:[0,1]
	v_pk_add_f32 v[48:49], v[34:35], v[38:39] op_sel_hi:[1,0] neg_lo:[0,1] neg_hi:[0,1]
	v_pk_add_f32 v[52:53], v[30:31], v[38:39] op_sel_hi:[1,0] neg_lo:[0,1] neg_hi:[0,1]
	v_pk_mul_f32 v[30:31], v[46:47], v[46:47]
	v_pk_mul_f32 v[32:33], v[48:49], v[48:49]
	v_add_f32_e32 v30, v30, v31
	v_pk_add_f32 v[50:51], v[36:37], v[38:39] op_sel_hi:[1,0] neg_lo:[0,1] neg_hi:[0,1]
	v_add_f32_e32 v30, v30, v32
	v_pk_mul_f32 v[34:35], v[50:51], v[50:51]
	v_add_f32_e32 v30, v30, v33
	v_add_f32_e32 v30, v30, v34
	v_pk_mul_f32 v[36:37], v[52:53], v[52:53]
	v_add_f32_e32 v30, v30, v35
	v_add_f32_e32 v30, v30, v36
	v_add_f32_e32 v30, v30, v37
	s_waitcnt vmcnt(5)
	v_pk_mul_f32 v[6:7], v[6:7], v[46:47]
	v_add_f32_dpp v30, v30, v30 quad_perm:[1,0,3,2] row_mask:0xf bank_mask:0xf bound_ctrl:1
	v_pk_mul_f32 v[8:9], v[8:9], v[48:49]
	s_nop 0
	v_add_f32_dpp v30, v30, v30 quad_perm:[2,3,0,1] row_mask:0xf bank_mask:0xf bound_ctrl:1
	s_nop 1
	v_add_f32_dpp v30, v30, v30 row_half_mirror row_mask:0xf bank_mask:0xf bound_ctrl:1
	s_nop 1
	v_add_f32_dpp v30, v30, v30 row_mirror row_mask:0xf bank_mask:0xf bound_ctrl:1
	s_nop 0
	v_readlane_b32 s12, v30, 16
	v_readlane_b32 s13, v30, 48
	v_readlane_b32 s0, v30, 0
	v_readlane_b32 s1, v30, 32
	v_mov_b32_e32 v30, s12
	v_mov_b32_e32 v31, s13
	v_pk_add_f32 v[30:31], s[0:1], v[30:31]
	s_nop 0
	v_add_f32_e32 v30, v30, v31
	v_fmamk_f32 v30, v30, 0x3b000000, v61
	v_mul_f32_e32 v31, 0x4f800000, v30
	v_cmp_gt_f32_e32 vcc, s16, v30
	s_nop 1
	v_cndmask_b32_e32 v54, v30, v31, vcc
	v_sqrt_f32_e32 v38, v54
	global_load_dwordx4 v[30:33], v0, s[8:9]
	global_load_dwordx4 v[34:37], v0, s[10:11]
	v_add_u32_e32 v39, -1, v38
	v_add_u32_e32 v56, 1, v38
	v_fma_f32 v40, -v39, v38, v54
	v_fma_f32 v41, -v56, v38, v54
	v_cmp_ge_f32_e64 s[0:1], 0, v40
	s_nop 1
	v_cndmask_b32_e64 v57, v38, v39, s[0:1]
	v_cmp_lt_f32_e64 s[0:1], 0, v41
	global_load_dwordx4 v[38:41], v0, s[8:9] offset:1024
	global_load_dwordx4 v[42:45], v0, s[10:11] offset:1024
	v_cndmask_b32_e64 v46, v57, v56, s[0:1]
	v_mul_f32_e32 v47, 0x37800000, v46
	v_cndmask_b32_e32 v46, v46, v47, vcc
	v_cmp_class_f32_e32 vcc, v54, v55
	s_nop 1
	v_cndmask_b32_e32 v46, v46, v54, vcc
	v_div_scale_f32 v47, s[0:1], v46, v46, 1.0
	v_rcp_f32_e32 v54, v47
	v_div_scale_f32 v48, vcc, 1.0, v46, 1.0
	v_fma_f32 v49, -v47, v54, 1.0
	v_fmac_f32_e32 v54, v49, v54
	v_mul_f32_e32 v49, v48, v54
	v_fma_f32 v56, -v47, v49, v48
	v_fmac_f32_e32 v49, v56, v54
	v_fma_f32 v47, -v47, v49, v48
	v_div_fmas_f32 v47, v47, v54, v49
	v_div_fixup_f32 v46, v47, v46, 1.0
	s_waitcnt vmcnt(8)
	v_pk_fma_f32 v[6:7], v[46:47], v[6:7], v[10:11] op_sel_hi:[0,1,1]
	s_waitcnt vmcnt(5)
	v_pk_add_f32 v[6:7], v[6:7], v[22:23]
	v_pk_fma_f32 v[8:9], v[46:47], v[8:9], v[12:13] op_sel_hi:[0,1,1]
	v_pk_mul_f32 v[10:11], v[14:15], v[50:51]
	v_add_f32_e32 v14, 0, v6
	v_add_f32_e32 v14, v14, v7
	v_pk_add_f32 v[8:9], v[8:9], v[24:25]
	v_pk_fma_f32 v[10:11], v[46:47], v[10:11], v[18:19] op_sel_hi:[0,1,1]
	v_add_f32_e32 v14, v14, v8
	v_pk_mul_f32 v[12:13], v[16:17], v[52:53]
	v_add_f32_e32 v14, v14, v9
	s_waitcnt vmcnt(4)
	v_pk_add_f32 v[10:11], v[10:11], v[26:27]
	v_pk_fma_f32 v[12:13], v[46:47], v[12:13], v[20:21] op_sel_hi:[0,1,1]
	v_add_f32_e32 v14, v14, v10
	v_add_f32_e32 v14, v14, v11
	v_pk_add_f32 v[12:13], v[12:13], v[28:29]
	s_nop 0
	v_add_f32_e32 v14, v14, v12
	v_add_f32_e32 v14, v14, v13
	s_nop 1
	v_add_f32_dpp v14, v14, v14 quad_perm:[1,0,3,2] row_mask:0xf bank_mask:0xf bound_ctrl:1
	s_nop 1
	v_add_f32_dpp v14, v14, v14 quad_perm:[2,3,0,1] row_mask:0xf bank_mask:0xf bound_ctrl:1
	s_nop 1
	v_add_f32_dpp v14, v14, v14 row_half_mirror row_mask:0xf bank_mask:0xf bound_ctrl:1
	s_nop 1
	v_add_f32_dpp v14, v14, v14 row_mirror row_mask:0xf bank_mask:0xf bound_ctrl:1
	s_nop 0
	v_readlane_b32 s8, v14, 16
	v_readlane_b32 s9, v14, 48
	v_readlane_b32 s0, v14, 0
	v_readlane_b32 s1, v14, 32
	v_mov_b32_e32 v14, s8
	v_mov_b32_e32 v15, s9
	v_pk_add_f32 v[14:15], s[0:1], v[14:15]
	s_nop 0
	v_add_f32_e32 v14, v14, v15
	v_mul_f32_e32 v14, 0x3b000000, v14
	v_pk_add_f32 v[6:7], v[6:7], v[14:15] op_sel_hi:[1,0] neg_lo:[0,1] neg_hi:[0,1]
	v_pk_add_f32 v[8:9], v[8:9], v[14:15] op_sel_hi:[1,0] neg_lo:[0,1] neg_hi:[0,1]
	v_pk_mul_f32 v[16:17], v[6:7], v[6:7]
	v_pk_mul_f32 v[18:19], v[8:9], v[8:9]
	v_add_f32_e32 v16, v16, v17
	v_pk_add_f32 v[10:11], v[10:11], v[14:15] op_sel_hi:[1,0] neg_lo:[0,1] neg_hi:[0,1]
	v_add_f32_e32 v16, v16, v18
	v_pk_mul_f32 v[20:21], v[10:11], v[10:11]
	v_add_f32_e32 v16, v16, v19
	v_pk_add_f32 v[12:13], v[12:13], v[14:15] op_sel_hi:[1,0] neg_lo:[0,1] neg_hi:[0,1]
	v_add_f32_e32 v16, v16, v20
	v_pk_mul_f32 v[14:15], v[12:13], v[12:13]
	v_add_f32_e32 v16, v16, v21
	v_add_f32_e32 v14, v16, v14
	v_add_f32_e32 v14, v14, v15
	s_nop 1
	v_add_f32_dpp v14, v14, v14 quad_perm:[1,0,3,2] row_mask:0xf bank_mask:0xf bound_ctrl:1
	s_nop 1
	v_add_f32_dpp v14, v14, v14 quad_perm:[2,3,0,1] row_mask:0xf bank_mask:0xf bound_ctrl:1
	s_nop 1
	v_add_f32_dpp v14, v14, v14 row_half_mirror row_mask:0xf bank_mask:0xf bound_ctrl:1
	s_nop 1
	v_add_f32_dpp v14, v14, v14 row_mirror row_mask:0xf bank_mask:0xf bound_ctrl:1
	s_nop 0
	v_readlane_b32 s8, v14, 16
	v_readlane_b32 s9, v14, 48
	v_readlane_b32 s0, v14, 0
	v_readlane_b32 s1, v14, 32
	v_mov_b32_e32 v14, s8
	v_mov_b32_e32 v15, s9
	v_pk_add_f32 v[14:15], s[0:1], v[14:15]
	s_nop 0
	v_add_f32_e32 v14, v14, v15
	v_fmac_f32_e32 v61, 0x3b000000, v14
	v_mul_f32_e32 v14, 0x4f800000, v61
	v_cmp_gt_f32_e32 vcc, s16, v61
	s_nop 1
	v_cndmask_b32_e32 v14, v61, v14, vcc
	v_sqrt_f32_e32 v15, v14
	s_nop 0
	v_add_u32_e32 v16, -1, v15
	v_fma_f32 v17, -v16, v15, v14
	v_cmp_ge_f32_e64 s[0:1], 0, v17
	v_add_u32_e32 v17, 1, v15
	s_nop 0
	v_cndmask_b32_e64 v16, v15, v16, s[0:1]
	v_fma_f32 v15, -v17, v15, v14
	v_cmp_lt_f32_e64 s[0:1], 0, v15
	s_nop 1
	v_cndmask_b32_e64 v15, v16, v17, s[0:1]
	v_mul_f32_e32 v16, 0x37800000, v15
	v_cndmask_b32_e32 v15, v15, v16, vcc
	v_cmp_class_f32_e32 vcc, v14, v55
	s_nop 1
	v_cndmask_b32_e32 v16, v15, v14, vcc
	v_div_scale_f32 v17, s[0:1], v16, v16, 1.0
	v_rcp_f32_e32 v18, v17
	v_lshl_add_u64 v[14:15], v[4:5], 0, v[0:1]
	s_mov_b32 s0, 0x43000000
	v_fma_f32 v0, -v17, v18, 1.0
	v_fmac_f32_e32 v18, v0, v18
	v_div_scale_f32 v0, vcc, 1.0, v16, 1.0
	v_mul_f32_e32 v4, v0, v18
	v_fma_f32 v5, -v17, v4, v0
	v_fmac_f32_e32 v4, v5, v18
	v_fma_f32 v0, -v17, v4, v0
	v_div_fmas_f32 v0, v0, v18, v4
	v_div_fixup_f32 v0, v0, v16, 1.0
	s_waitcnt vmcnt(3)
	v_pk_mul_f32 v[4:5], v[30:31], v[6:7]
	v_pk_mul_f32 v[6:7], v[32:33], v[8:9]
	s_waitcnt vmcnt(2)
	v_pk_fma_f32 v[4:5], v[0:1], v[4:5], v[34:35] op_sel_hi:[0,1,1]
	s_waitcnt vmcnt(1)
	v_pk_mul_f32 v[8:9], v[38:39], v[10:11]
	v_pk_fma_f32 v[6:7], v[0:1], v[6:7], v[36:37] op_sel_hi:[0,1,1]
	s_waitcnt vmcnt(0)
	v_pk_fma_f32 v[8:9], v[0:1], v[8:9], v[42:43] op_sel_hi:[0,1,1]
	v_pk_mul_f32 v[10:11], v[40:41], v[12:13]
	v_fma_mixlo_f16 v12, v4, s0, 0
	v_pk_fma_f32 v[10:11], v[0:1], v[10:11], v[44:45] op_sel_hi:[0,1,1]
	global_store_dwordx4 v[14:15], v[4:7], off sc1
	global_store_dwordx4 v[14:15], v[8:11], off offset:1024 sc1
	v_mul_f32_e32 v0, 0x43000000, v4
	v_fma_mixlo_f16 v4, v4, s0, -v12 op_sel_hi:[0,0,1]
	v_fma_mixlo_f16 v12, v8, s0, 0
	v_mul_f32_e32 v13, 0x43000000, v8
	v_fma_mixlo_f16 v8, v8, s0, -v12 op_sel_hi:[0,0,1]
	v_mul_f32_e32 v12, 0x43000000, v5
	v_fma_mixlo_f16 v14, v5, s0, 0
	v_cvt_pk_f16_f32 v12, v0, v12
	v_mul_f32_e32 v0, 0x43000000, v9
	v_pk_mul_f32 v[16:17], v[6:7], s[0:1] op_sel_hi:[1,0]
	v_fma_mixhi_f16 v4, v5, s0, -v14 op_sel_hi:[0,0,1]
	v_cvt_pk_f16_f32 v14, v13, v0
	v_cvt_pk_f16_f32 v13, v16, v17
	v_pk_mul_f32 v[18:19], v[10:11], s[0:1] op_sel_hi:[1,0]
	v_cvt_f32_f16_e32 v16, v13
	v_cvt_f32_f16_sdwa v17, v13 dst_sel:DWORD dst_unused:UNUSED_PAD src0_sel:WORD_1
	v_cvt_pk_f16_f32 v15, v18, v19
	v_cvt_f32_f16_e32 v18, v15
	v_cvt_f32_f16_sdwa v19, v15 dst_sel:DWORD dst_unused:UNUSED_PAD src0_sel:WORD_1
	v_fma_mixlo_f16 v5, v9, s0, 0
	v_pk_fma_f32 v[6:7], v[6:7], s[0:1], v[16:17] op_sel_hi:[1,0,1] neg_lo:[0,0,1] neg_hi:[0,0,1]
	v_fma_mixhi_f16 v8, v9, s0, -v5 op_sel_hi:[0,0,1]
	v_cvt_pk_f16_f32 v5, v6, v7
	v_pk_fma_f32 v[6:7], v[10:11], s[0:1], v[18:19] op_sel_hi:[1,0,1] neg_lo:[0,0,1] neg_hi:[0,0,1]
	v_lshlrev_b32_e32 v0, 1, v60
	v_cvt_pk_f16_f32 v9, v6, v7
	v_lshl_add_u64 v[6:7], s[6:7], 0, v[2:3]
	v_lshl_add_u64 v[2:3], s[2:3], 0, v[2:3]
	v_lshl_add_u64 v[6:7], v[6:7], 0, v[0:1]
	v_lshl_add_u64 v[0:1], v[2:3], 0, v[0:1]
	global_store_dwordx2 v[6:7], v[12:13], off
	global_store_dwordx2 v[6:7], v[14:15], off offset:512
	global_store_dwordx2 v[0:1], v[4:5], off
	global_store_dwordx2 v[0:1], v[8:9], off offset:512
	s_endpgm
	s_endpgm
	s_endpgm
	s_endpgm
	s_endpgm
	s_endpgm
	s_endpgm
	s_endpgm
	s_endpgm
	s_endpgm
	s_endpgm
	s_endpgm
	s_endpgm
	s_endpgm
	s_endpgm
	s_endpgm
	s_endpgm
	s_endpgm
	s_endpgm
	s_endpgm
	s_endpgm
	s_endpgm
	s_endpgm
	s_endpgm
	s_endpgm
	s_endpgm
	s_endpgm
	s_endpgm
	s_endpgm
	s_endpgm
	s_endpgm
	s_endpgm
	s_endpgm
	s_endpgm
	s_endpgm
	s_endpgm
	s_endpgm
	s_endpgm
	s_endpgm
	s_endpgm
	s_endpgm
	s_endpgm
	s_endpgm
	s_endpgm
	s_endpgm
	s_endpgm
	s_endpgm
	s_endpgm
	s_endpgm
	.section	.rodata,"a",@progbits
	.p2align	6, 0x0

_Z9ln_kernelILi1ELi8EEvPKflS1_S1_S1_S1_S1_S1_S1_PfPDF16_S3_iii:
	s_bitcmp1_b32 s2, 8
	s_cbranch_scc0 .Lprio_skip_q4
	s_setprio 1

.LBB15_5:
	v_lshlrev_b32_e32 v0, 2, v0
	v_and_b32_e32 v8, 0xfc, v0
	v_lshlrev_b64 v[4:5], 11, v[4:5]
	v_lshlrev_b32_e32 v0, 2, v8
	v_mov_b32_e32 v1, 0
	s_waitcnt lgkmcnt(0)
	v_lshl_add_u64 v[4:5], s[24:25], 0, v[4:5]
	v_lshl_add_u64 v[4:5], v[4:5], 0, v[0:1]
	global_load_dwordx4 v[10:13], v[4:5], off
	global_load_dwordx4 v[14:17], v0, s[20:21]
	global_load_dwordx4 v[18:21], v0, s[20:21] offset:1024
	global_load_dwordx4 v[22:25], v[4:5], off offset:1024
	s_load_dwordx2 s[0:1], s[0:1], 0x8
	v_lshlrev_b64 v[4:5], 11, v[2:3]
	v_lshl_add_u64 v[50:51], s[22:23], 0, v[4:5]
	v_lshl_add_u64 v[30:31], v[50:51], 0, v[0:1]
	global_load_dwordx4 v[26:29], v[30:31], off
	s_waitcnt lgkmcnt(0)
	v_lshl_add_u64 v[34:35], s[0:1], 2, v[50:51]
	global_load_dwordx4 v[30:33], v[30:31], off offset:1024
	v_lshl_add_u64 v[42:43], v[34:35], 0, v[0:1]
	global_load_dwordx4 v[34:37], v[42:43], off
	global_load_dwordx4 v[38:41], v[42:43], off offset:1024
	v_lshl_add_u64 v[42:43], s[0:1], 3, v[50:51]
	v_lshl_add_u64 v[52:53], v[42:43], 0, v[0:1]
	global_load_dwordx4 v[42:45], v[52:53], off
	global_load_dwordx4 v[46:49], v[52:53], off offset:1024
	v_mad_u64_u32 v[52:53], s[16:17], s0, 12, v[50:51]
	v_mad_u64_u32 v[56:57], s[16:17], s0, 20, v[50:51]
	v_mad_u64_u32 v[62:63], s[16:17], s0, 24, v[50:51]
	v_lshl_add_u64 v[54:55], s[0:1], 4, v[50:51]
	v_mad_u64_u32 v[50:51], s[16:17], s0, 28, v[50:51]
	v_lshl_add_u64 v[54:55], v[54:55], 0, v[0:1]
	v_lshlrev_b64 v[6:7], 11, v[6:7]
	v_lshl_add_u64 v[6:7], s[18:19], 0, v[6:7]
	v_lshl_add_u64 v[6:7], v[6:7], 0, v[0:1]
	v_lshl_add_u64 v[4:5], s[4:5], 0, v[4:5]
	v_lshlrev_b64 v[2:3], 10, v[2:3]
	s_waitcnt vmcnt(8)
	v_pk_add_f32 v[58:59], v[14:15], v[10:11]
	v_mov_b32_e32 v10, v53
	v_pk_add_f32 v[60:61], v[16:17], v[12:13]
	v_mov_b32_e32 v12, v57
	v_mad_u64_u32 v[10:11], s[16:17], s1, 12, v[10:11]
	v_mov_b32_e32 v53, v10
	v_mov_b32_e32 v10, v63
	v_mad_u64_u32 v[12:13], s[16:17], s1, 20, v[12:13]
	v_mov_b32_e32 v57, v12
	v_mov_b32_e32 v12, v51
	v_mad_u64_u32 v[10:11], s[16:17], s1, 24, v[10:11]
	s_waitcnt vmcnt(6)
	v_pk_add_f32 v[66:67], v[18:19], v[22:23]
	v_lshl_add_u64 v[22:23], v[52:53], 0, v[0:1]
	v_mad_u64_u32 v[64:65], s[0:1], s1, 28, v[12:13]
	v_mov_b32_e32 v63, v10
	v_pk_add_f32 v[68:69], v[20:21], v[24:25]
	global_load_dwordx4 v[10:13], v[54:55], off
	global_load_dwordx4 v[14:17], v[54:55], off offset:1024
	global_load_dwordx4 v[18:21], v[22:23], off
	v_lshl_add_u64 v[52:53], v[56:57], 0, v[0:1]
	s_waitcnt vmcnt(8)
	v_pk_add_f32 v[54:55], v[58:59], v[26:27]
	v_pk_add_f32 v[56:57], v[60:61], v[28:29]
	global_load_dwordx4 v[26:29], v[52:53], off
	v_lshl_add_u64 v[58:59], v[62:63], 0, v[0:1]
	global_load_dwordx4 v[22:25], v[22:23], off offset:1024
	v_mov_b32_e32 v51, v64
	s_waitcnt vmcnt(9)
	v_pk_add_f32 v[60:61], v[66:67], v[30:31]
	v_pk_add_f32 v[62:63], v[68:69], v[32:33]
	s_waitcnt vmcnt(8)
	v_pk_add_f32 v[54:55], v[54:55], v[34:35]
	v_pk_add_f32 v[56:57], v[56:57], v[36:37]
	global_load_dwordx4 v[30:33], v[52:53], off offset:1024
	global_load_dwordx4 v[34:37], v[58:59], off
	v_lshl_add_u64 v[50:51], v[50:51], 0, v[0:1]
	s_waitcnt vmcnt(9)
	v_pk_add_f32 v[52:53], v[60:61], v[38:39]
	v_pk_add_f32 v[60:61], v[62:63], v[40:41]
	s_waitcnt vmcnt(8)
	v_pk_add_f32 v[54:55], v[54:55], v[42:43]
	v_pk_add_f32 v[56:57], v[56:57], v[44:45]
	global_load_dwordx4 v[38:41], v[50:51], off
	global_load_dwordx4 v[42:45], v[58:59], off offset:1024
	s_waitcnt vmcnt(9)
	v_pk_add_f32 v[52:53], v[52:53], v[46:47]
	v_pk_add_f32 v[58:59], v[60:61], v[48:49]
	global_load_dwordx4 v[46:49], v[50:51], off offset:1024
	s_waitcnt vmcnt(7)
	v_pk_add_f32 v[18:19], v[54:55], v[18:19]
	s_nop 0
	v_pk_add_f32 v[10:11], v[18:19], v[10:11]
	v_pk_add_f32 v[20:21], v[56:57], v[20:21]
	v_mov_b32_e32 v57, 0x3727c5ac
	s_waitcnt vmcnt(6)
	v_pk_add_f32 v[18:19], v[10:11], v[26:27]
	v_pk_add_f32 v[12:13], v[20:21], v[12:13]
	s_waitcnt vmcnt(5)
	v_pk_add_f32 v[22:23], v[52:53], v[22:23]
	v_pk_add_f32 v[10:11], v[58:59], v[24:25]
	v_pk_add_f32 v[14:15], v[22:23], v[14:15]
	v_pk_add_f32 v[10:11], v[10:11], v[16:17]
	v_pk_add_f32 v[20:21], v[12:13], v[28:29]
	v_mov_b32_e32 v58, 0x260
	s_waitcnt vmcnt(4)
	v_pk_add_f32 v[50:51], v[14:15], v[30:31]
	v_pk_add_f32 v[52:53], v[10:11], v[32:33]
	global_load_dwordx4 v[10:13], v0, s[12:13]
	global_load_dwordx4 v[14:17], v0, s[14:15]
	s_waitcnt vmcnt(5)
	v_pk_add_f32 v[18:19], v[18:19], v[34:35]
	s_waitcnt vmcnt(4)
	v_pk_add_f32 v[34:35], v[18:19], v[38:39]
	v_pk_add_f32 v[18:19], v[20:21], v[36:37]
	v_add_f32_e32 v9, 0, v34
	v_pk_add_f32 v[36:37], v[18:19], v[40:41]
	global_load_dwordx4 v[18:21], v0, s[12:13] offset:1024
	global_load_dwordx4 v[22:25], v0, s[14:15] offset:1024
	global_load_dwordx4 v[26:29], v[6:7], off
	global_load_dwordx4 v[30:33], v[6:7], off offset:1024
	v_add_f32_e32 v9, v9, v35
	v_add_f32_e32 v9, v9, v36
	s_waitcnt vmcnt(7)
	v_pk_add_f32 v[6:7], v[50:51], v[42:43]
	v_add_f32_e32 v9, v9, v37
	s_waitcnt vmcnt(6)
	v_pk_add_f32 v[6:7], v[6:7], v[46:47]
	v_pk_add_f32 v[38:39], v[52:53], v[44:45]
	v_add_f32_e32 v9, v9, v6
	v_add_f32_e32 v9, v9, v7
	v_pk_add_f32 v[38:39], v[38:39], v[48:49]
	s_nop 0
	v_add_f32_e32 v9, v9, v38
	v_add_f32_e32 v9, v9, v39
	s_nop 1
	v_add_f32_dpp v9, v9, v9 quad_perm:[1,0,3,2] row_mask:0xf bank_mask:0xf bound_ctrl:1
	s_nop 1
	v_add_f32_dpp v9, v9, v9 quad_perm:[2,3,0,1] row_mask:0xf bank_mask:0xf bound_ctrl:1
	s_nop 1
	v_add_f32_dpp v9, v9, v9 row_half_mirror row_mask:0xf bank_mask:0xf bound_ctrl:1
	s_nop 1
	v_add_f32_dpp v9, v9, v9 row_mirror row_mask:0xf bank_mask:0xf bound_ctrl:1
	s_nop 0
	v_readlane_b32 s12, v9, 16
	v_readlane_b32 s13, v9, 48
	v_readlane_b32 s0, v9, 0
	v_readlane_b32 s1, v9, 32
	v_mov_b32_e32 v40, s12
	v_mov_b32_e32 v41, s13
	v_pk_add_f32 v[40:41], s[0:1], v[40:41]
	s_nop 0
	v_add_f32_e32 v9, v40, v41
	v_mul_f32_e32 v40, 0x3b000000, v9
	v_pk_add_f32 v[50:51], v[34:35], v[40:41] op_sel_hi:[1,0] neg_lo:[0,1] neg_hi:[0,1]
	v_pk_add_f32 v[52:53], v[36:37], v[40:41] op_sel_hi:[1,0] neg_lo:[0,1] neg_hi:[0,1]
	v_pk_mul_f32 v[34:35], v[50:51], v[50:51]
	v_pk_mul_f32 v[36:37], v[52:53], v[52:53]
	v_add_f32_e32 v9, v34, v35
	v_pk_add_f32 v[6:7], v[6:7], v[40:41] op_sel_hi:[1,0] neg_lo:[0,1] neg_hi:[0,1]
	v_add_f32_e32 v9, v9, v36
	v_pk_mul_f32 v[42:43], v[6:7], v[6:7]
	v_add_f32_e32 v9, v9, v37
	v_pk_add_f32 v[54:55], v[38:39], v[40:41] op_sel_hi:[1,0] neg_lo:[0,1] neg_hi:[0,1]
	v_add_f32_e32 v9, v9, v42
	v_pk_mul_f32 v[38:39], v[54:55], v[54:55]
	v_add_f32_e32 v9, v9, v43
	v_add_f32_e32 v9, v9, v38
	v_add_f32_e32 v9, v9, v39
	s_waitcnt vmcnt(5)
	v_pk_mul_f32 v[10:11], v[10:11], v[50:51]
	v_add_f32_dpp v9, v9, v9 quad_perm:[1,0,3,2] row_mask:0xf bank_mask:0xf bound_ctrl:1
	v_pk_mul_f32 v[12:13], v[12:13], v[52:53]
	s_waitcnt vmcnt(3)
	v_pk_mul_f32 v[6:7], v[18:19], v[6:7]
	v_add_f32_dpp v9, v9, v9 quad_perm:[2,3,0,1] row_mask:0xf bank_mask:0xf bound_ctrl:1
	s_nop 1
	v_add_f32_dpp v9, v9, v9 row_half_mirror row_mask:0xf bank_mask:0xf bound_ctrl:1
	s_nop 1
	v_add_f32_dpp v9, v9, v9 row_mirror row_mask:0xf bank_mask:0xf bound_ctrl:1
	s_nop 0
	v_readlane_b32 s12, v9, 16
	v_readlane_b32 s13, v9, 48
	v_readlane_b32 s0, v9, 0
	v_readlane_b32 s1, v9, 32
	v_mov_b32_e32 v34, s12
	v_mov_b32_e32 v35, s13
	v_pk_add_f32 v[34:35], s[0:1], v[34:35]
	s_mov_b32 s12, 0xf800000
	v_add_f32_e32 v9, v34, v35
	v_fmamk_f32 v9, v9, 0x3b000000, v57
	v_mul_f32_e32 v34, 0x4f800000, v9
	v_cmp_gt_f32_e32 vcc, s12, v9
	s_nop 1
	v_cndmask_b32_e32 v9, v9, v34, vcc
	v_sqrt_f32_e32 v34, v9
	s_nop 0
	v_add_u32_e32 v35, -1, v34
	v_fma_f32 v36, -v35, v34, v9
	v_cmp_ge_f32_e64 s[0:1], 0, v36
	v_add_u32_e32 v36, 1, v34
	s_nop 0
	v_cndmask_b32_e64 v35, v34, v35, s[0:1]
	v_fma_f32 v34, -v36, v34, v9
	v_cmp_lt_f32_e64 s[0:1], 0, v34
	s_nop 1
	v_cndmask_b32_e64 v34, v35, v36, s[0:1]
	v_mul_f32_e32 v35, 0x37800000, v34
	v_cndmask_b32_e32 v34, v34, v35, vcc
	v_cmp_class_f32_e32 vcc, v9, v58
	s_nop 1
	v_cndmask_b32_e32 v9, v34, v9, vcc
	v_div_scale_f32 v42, s[0:1], v9, v9, 1.0
	v_rcp_f32_e32 v43, v42
	global_load_dwordx4 v[34:37], v0, s[8:9]
	global_load_dwordx4 v[38:41], v0, s[10:11]
	v_fma_f32 v44, -v42, v43, 1.0
	v_fmac_f32_e32 v43, v44, v43
	v_div_scale_f32 v44, vcc, 1.0, v9, 1.0
	v_mul_f32_e32 v45, v44, v43
	v_fma_f32 v46, -v42, v45, v44
	v_fmac_f32_e32 v45, v46, v43
	v_fma_f32 v42, -v42, v45, v44
	v_div_fmas_f32 v56, v42, v43, v45
	global_load_dwordx4 v[42:45], v0, s[8:9] offset:1024
	global_load_dwordx4 v[46:49], v0, s[10:11] offset:1024
	v_div_fixup_f32 v56, v56, v9, 1.0
	v_pk_fma_f32 v[10:11], v[56:57], v[10:11], v[14:15] op_sel_hi:[0,1,1]
	s_waitcnt vmcnt(5)
	v_pk_add_f32 v[10:11], v[10:11], v[26:27]
	v_pk_fma_f32 v[12:13], v[56:57], v[12:13], v[16:17] op_sel_hi:[0,1,1]
	v_add_f32_e32 v9, 0, v10
	v_add_f32_e32 v9, v9, v11
	v_pk_add_f32 v[12:13], v[12:13], v[28:29]
	v_pk_fma_f32 v[6:7], v[56:57], v[6:7], v[22:23] op_sel_hi:[0,1,1]
	v_add_f32_e32 v9, v9, v12
	v_pk_mul_f32 v[14:15], v[20:21], v[54:55]
	v_add_f32_e32 v9, v9, v13
	s_waitcnt vmcnt(4)
	v_pk_add_f32 v[6:7], v[6:7], v[30:31]
	v_pk_fma_f32 v[14:15], v[56:57], v[14:15], v[24:25] op_sel_hi:[0,1,1]
	v_add_f32_e32 v9, v9, v6
	v_add_f32_e32 v9, v9, v7
	v_pk_add_f32 v[14:15], v[14:15], v[32:33]
	s_nop 0
	v_add_f32_e32 v9, v9, v14
	v_add_f32_e32 v9, v9, v15
	s_nop 1
	v_add_f32_dpp v9, v9, v9 quad_perm:[1,0,3,2] row_mask:0xf bank_mask:0xf bound_ctrl:1
	s_nop 1
	v_add_f32_dpp v9, v9, v9 quad_perm:[2,3,0,1] row_mask:0xf bank_mask:0xf bound_ctrl:1
	s_nop 1
	v_add_f32_dpp v9, v9, v9 row_half_mirror row_mask:0xf bank_mask:0xf bound_ctrl:1
	s_nop 1
	v_add_f32_dpp v9, v9, v9 row_mirror row_mask:0xf bank_mask:0xf bound_ctrl:1
	s_nop 0
	v_readlane_b32 s8, v9, 16
	v_readlane_b32 s9, v9, 48
	v_readlane_b32 s0, v9, 0
	v_readlane_b32 s1, v9, 32
	v_mov_b32_e32 v16, s8
	v_mov_b32_e32 v17, s9
	v_pk_add_f32 v[16:17], s[0:1], v[16:17]
	s_nop 0
	v_add_f32_e32 v9, v16, v17
	v_mul_f32_e32 v16, 0x3b000000, v9
	v_pk_add_f32 v[10:11], v[10:11], v[16:17] op_sel_hi:[1,0] neg_lo:[0,1] neg_hi:[0,1]
	v_pk_add_f32 v[12:13], v[12:13], v[16:17] op_sel_hi:[1,0] neg_lo:[0,1] neg_hi:[0,1]
	v_pk_mul_f32 v[18:19], v[10:11], v[10:11]
	v_pk_mul_f32 v[20:21], v[12:13], v[12:13]
	v_add_f32_e32 v9, v18, v19
	v_pk_add_f32 v[22:23], v[6:7], v[16:17] op_sel_hi:[1,0] neg_lo:[0,1] neg_hi:[0,1]
	v_add_f32_e32 v9, v9, v20
	v_pk_mul_f32 v[6:7], v[22:23], v[22:23]
	v_add_f32_e32 v9, v9, v21
	v_pk_add_f32 v[14:15], v[14:15], v[16:17] op_sel_hi:[1,0] neg_lo:[0,1] neg_hi:[0,1]
	v_add_f32_e32 v6, v9, v6
	v_pk_mul_f32 v[16:17], v[14:15], v[14:15]
	v_add_f32_e32 v6, v6, v7
	v_add_f32_e32 v6, v6, v16
	v_add_f32_e32 v6, v6, v17
	s_nop 1
	v_add_f32_dpp v6, v6, v6 quad_perm:[1,0,3,2] row_mask:0xf bank_mask:0xf bound_ctrl:1
	s_nop 1
	v_add_f32_dpp v6, v6, v6 quad_perm:[2,3,0,1] row_mask:0xf bank_mask:0xf bound_ctrl:1
	s_nop 1
	v_add_f32_dpp v6, v6, v6 row_half_mirror row_mask:0xf bank_mask:0xf bound_ctrl:1
	s_nop 1
	v_add_f32_dpp v6, v6, v6 row_mirror row_mask:0xf bank_mask:0xf bound_ctrl:1
	s_nop 0
	v_readlane_b32 s8, v6, 16
	v_readlane_b32 s9, v6, 48
	v_readlane_b32 s0, v6, 0
	v_readlane_b32 s1, v6, 32
	v_mov_b32_e32 v6, s8
	v_mov_b32_e32 v7, s9
	v_pk_add_f32 v[6:7], s[0:1], v[6:7]
	s_nop 0
	v_add_f32_e32 v6, v6, v7
	v_fmac_f32_e32 v57, 0x3b000000, v6
	v_mul_f32_e32 v6, 0x4f800000, v57
	v_cmp_gt_f32_e32 vcc, s12, v57
	s_nop 1
	v_cndmask_b32_e32 v6, v57, v6, vcc
	v_sqrt_f32_e32 v7, v6
	s_nop 0
	v_add_u32_e32 v9, -1, v7
	v_fma_f32 v16, -v9, v7, v6
	v_cmp_ge_f32_e64 s[0:1], 0, v16
	v_add_u32_e32 v16, 1, v7
	s_nop 0
	v_cndmask_b32_e64 v9, v7, v9, s[0:1]
	v_fma_f32 v7, -v16, v7, v6
	v_cmp_lt_f32_e64 s[0:1], 0, v7
	s_nop 1
	v_cndmask_b32_e64 v7, v9, v16, s[0:1]
	v_mul_f32_e32 v9, 0x37800000, v7
	v_cndmask_b32_e32 v7, v7, v9, vcc
	v_cmp_class_f32_e32 vcc, v6, v58
	v_lshl_add_u64 v[16:17], v[4:5], 0, v[0:1]
	s_nop 0
	v_cndmask_b32_e32 v6, v7, v6, vcc
	v_div_scale_f32 v7, s[0:1], v6, v6, 1.0
	v_rcp_f32_e32 v9, v7
	s_mov_b32 s0, 0x43000000
	v_fma_f32 v0, -v7, v9, 1.0
	v_fmac_f32_e32 v9, v0, v9
	v_div_scale_f32 v0, vcc, 1.0, v6, 1.0
	v_mul_f32_e32 v4, v0, v9
	v_fma_f32 v5, -v7, v4, v0
	v_fmac_f32_e32 v4, v5, v9
	v_fma_f32 v0, -v7, v4, v0
	v_div_fmas_f32 v0, v0, v9, v4
	v_div_fixup_f32 v0, v0, v6, 1.0
	s_waitcnt vmcnt(3)
	v_pk_mul_f32 v[4:5], v[34:35], v[10:11]
	v_pk_mul_f32 v[6:7], v[36:37], v[12:13]
	s_waitcnt vmcnt(2)
	v_pk_fma_f32 v[4:5], v[0:1], v[4:5], v[38:39] op_sel_hi:[0,1,1]
	v_pk_fma_f32 v[6:7], v[0:1], v[6:7], v[40:41] op_sel_hi:[0,1,1]
	s_waitcnt vmcnt(1)
	v_pk_mul_f32 v[10:11], v[42:43], v[22:23]
	v_pk_mul_f32 v[12:13], v[44:45], v[14:15]
	v_fma_mixlo_f16 v9, v4, s0, 0
	s_waitcnt vmcnt(0)
	v_pk_fma_f32 v[10:11], v[0:1], v[10:11], v[46:47] op_sel_hi:[0,1,1]
	v_pk_fma_f32 v[12:13], v[0:1], v[12:13], v[48:49] op_sel_hi:[0,1,1]
	global_store_dwordx4 v[16:17], v[4:7], off sc1
	global_store_dwordx4 v[16:17], v[10:13], off offset:1024 sc1
	v_mul_f32_e32 v0, 0x43000000, v4
	v_fma_mixlo_f16 v4, v4, s0, -v9 op_sel_hi:[0,0,1]
	v_fma_mixlo_f16 v15, v5, s0, 0
	v_pk_mul_f32 v[18:19], v[6:7], s[0:1] op_sel_hi:[1,0]
	v_fma_mixhi_f16 v4, v5, s0, -v15 op_sel_hi:[0,0,1]
	v_cvt_pk_f16_f32 v15, v18, v19
	v_pk_mul_f32 v[20:21], v[12:13], s[0:1] op_sel_hi:[1,0]
	v_cvt_f32_f16_e32 v18, v15
	v_cvt_f32_f16_sdwa v19, v15 dst_sel:DWORD dst_unused:UNUSED_PAD src0_sel:WORD_1
	v_cvt_pk_f16_f32 v17, v20, v21
	v_cvt_f32_f16_e32 v20, v17
	v_cvt_f32_f16_sdwa v21, v17 dst_sel:DWORD dst_unused:UNUSED_PAD src0_sel:WORD_1
	v_fma_mixlo_f16 v14, v10, s0, 0
	v_mul_f32_e32 v9, 0x43000000, v10
	v_fma_mixlo_f16 v10, v10, s0, -v14 op_sel_hi:[0,0,1]
	v_mul_f32_e32 v14, 0x43000000, v5
	v_fma_mixlo_f16 v5, v11, s0, 0
	v_pk_fma_f32 v[6:7], v[6:7], s[0:1], v[18:19] op_sel_hi:[1,0,1] neg_lo:[0,0,1] neg_hi:[0,0,1]
	v_cvt_pk_f16_f32 v14, v0, v14
	v_mul_f32_e32 v0, 0x43000000, v11
	v_fma_mixhi_f16 v10, v11, s0, -v5 op_sel_hi:[0,0,1]
	v_cvt_pk_f16_f32 v5, v6, v7
	v_pk_fma_f32 v[6:7], v[12:13], s[0:1], v[20:21] op_sel_hi:[1,0,1] neg_lo:[0,0,1] neg_hi:[0,0,1]
	v_cvt_pk_f16_f32 v16, v9, v0
	v_cvt_pk_f16_f32 v11, v6, v7
	v_lshl_add_u64 v[6:7], s[6:7], 0, v[2:3]
	v_lshlrev_b32_e32 v0, 1, v8
	v_lshl_add_u64 v[2:3], s[2:3], 0, v[2:3]
	v_lshl_add_u64 v[6:7], v[6:7], 0, v[0:1]
	v_lshl_add_u64 v[0:1], v[2:3], 0, v[0:1]
	global_store_dwordx2 v[6:7], v[14:15], off
	global_store_dwordx2 v[6:7], v[16:17], off offset:512
	global_store_dwordx2 v[0:1], v[4:5], off
	global_store_dwordx2 v[0:1], v[10:11], off offset:512
	s_endpgm
	s_endpgm
	s_endpgm
	s_endpgm
	s_endpgm
	s_endpgm
	s_endpgm
	s_endpgm
	s_endpgm
	s_endpgm
	s_endpgm
	s_endpgm
	s_endpgm
	s_endpgm
	s_endpgm
	s_endpgm
	s_endpgm
	s_endpgm
	s_endpgm
	s_endpgm
	s_endpgm
	s_endpgm
	s_endpgm
	s_endpgm
	s_endpgm
	s_endpgm
	s_endpgm
	s_endpgm
	s_endpgm
	.section	.rodata,"a",@progbits
	.p2align	6, 0x0

_Z9ln_kernelILi0ELi1EEvPKflS1_S1_S1_S1_S1_S1_S1_PfPDF16_S3_iii:
	s_bitcmp1_b32 s2, 8
	s_cbranch_scc0 .Lprio_skip_q5
	s_setprio 1
.Lprio_skip_q5:
	s_load_dwordx4 s[12:15], s[0:1], 0x60
	s_load_dwordx2 s[16:17], s[0:1], 0x10
	s_load_dwordx4 s[4:7], s[0:1], 0x20
	v_lshrrev_b32_e32 v1, 6, v0
	v_lshl_or_b32 v6, s2, 2, v1
	s_waitcnt lgkmcnt(0)
	s_cmp_gt_i32 s13, -1
	v_ashrrev_i32_e32 v7, 31, v6
	s_cbranch_scc0 .LBB19_2
	s_ashr_i32 s2, s14, 31
	v_mov_b32_e32 v2, s14
	v_mov_b32_e32 v3, s2
	v_mad_u64_u32 v[2:3], s[2:3], s13, v6, v[2:3]
	v_mov_b32_e32 v4, v3
	v_mad_u64_u32 v[4:5], s[2:3], s13, v7, v[4:5]
	v_mov_b32_e32 v3, v4
	s_mov_b64 s[20:21], 0
	s_branch .LBB19_3

.LBB19_5:
	v_lshlrev_b32_e32 v0, 2, v0
	v_and_b32_e32 v50, 0xfc, v0
	v_lshlrev_b64 v[2:3], 11, v[2:3]
	v_lshlrev_b32_e32 v4, 2, v50
	v_mov_b32_e32 v5, 0
	s_waitcnt lgkmcnt(0)
	v_lshl_add_u64 v[2:3], s[14:15], 0, v[2:3]
	v_lshlrev_b64 v[36:37], 11, v[6:7]
	v_lshl_add_u64 v[2:3], v[2:3], 0, v[4:5]
	v_lshl_add_u64 v[0:1], s[18:19], 0, v[36:37]
	global_load_dwordx4 v[8:11], v[2:3], off
	global_load_dwordx4 v[12:15], v4, s[16:17]
	global_load_dwordx4 v[16:19], v4, s[16:17] offset:1024
	global_load_dwordx4 v[20:23], v[2:3], off offset:1024
	v_lshl_add_u64 v[38:39], v[0:1], 0, v[4:5]
	global_load_dwordx4 v[24:27], v[38:39], off
	global_load_dwordx4 v[28:31], v[38:39], off offset:1024
	global_load_dwordx4 v[32:35], v4, s[4:5]
	global_load_dwordx4 v[0:3], v4, s[4:5] offset:1024
	v_lshl_add_u64 v[36:37], s[8:9], 0, v[36:37]
	v_lshl_add_u64 v[48:49], v[36:37], 0, v[4:5]
	global_load_dwordx4 v[36:39], v4, s[6:7]
	global_load_dwordx4 v[40:43], v4, s[6:7] offset:1024
	v_lshlrev_b64 v[6:7], 10, v[6:7]
	v_lshl_add_u64 v[44:45], s[10:11], 0, v[6:7]
	v_lshl_add_u64 v[46:47], s[2:3], 0, v[6:7]
	v_mov_b32_e32 v51, 0x3727c5ac
	s_mov_b32 s5, 0xf800000
	v_mov_b32_e32 v52, 0x260
	s_mov_b32 s4, 0x43000000
	v_lshlrev_b32_e32 v4, 1, v50
	v_lshl_add_u64 v[44:45], v[44:45], 0, v[4:5]
	s_waitcnt vmcnt(8)
	v_pk_add_f32 v[6:7], v[12:13], v[8:9]
	s_waitcnt vmcnt(5)
	v_pk_add_f32 v[6:7], v[24:25], v[6:7]
	v_pk_add_f32 v[8:9], v[14:15], v[10:11]
	v_add_f32_e32 v14, 0, v6
	v_pk_add_f32 v[8:9], v[26:27], v[8:9]
	v_add_f32_e32 v14, v14, v7
	v_pk_add_f32 v[10:11], v[16:17], v[20:21]
	v_add_f32_e32 v14, v14, v8
	s_waitcnt vmcnt(4)
	v_pk_add_f32 v[10:11], v[28:29], v[10:11]
	v_add_f32_e32 v14, v14, v9
	v_pk_add_f32 v[12:13], v[18:19], v[22:23]
	v_add_f32_e32 v14, v14, v10
	v_pk_add_f32 v[12:13], v[30:31], v[12:13]
	v_add_f32_e32 v14, v14, v11
	v_add_f32_e32 v14, v14, v12
	v_add_f32_e32 v14, v14, v13
	s_nop 1
	v_add_f32_dpp v14, v14, v14 quad_perm:[1,0,3,2] row_mask:0xf bank_mask:0xf bound_ctrl:1
	s_nop 1
	v_add_f32_dpp v14, v14, v14 quad_perm:[2,3,0,1] row_mask:0xf bank_mask:0xf bound_ctrl:1
	s_nop 1
	v_add_f32_dpp v14, v14, v14 row_half_mirror row_mask:0xf bank_mask:0xf bound_ctrl:1
	s_nop 1
	v_add_f32_dpp v14, v14, v14 row_mirror row_mask:0xf bank_mask:0xf bound_ctrl:1
	s_nop 0
	v_readlane_b32 s2, v14, 16
	v_readlane_b32 s3, v14, 48
	v_readlane_b32 s0, v14, 0
	v_readlane_b32 s1, v14, 32
	v_mov_b32_e32 v14, s2
	v_mov_b32_e32 v15, s3
	v_pk_add_f32 v[14:15], s[0:1], v[14:15]
	s_nop 0
	v_add_f32_e32 v14, v14, v15
	v_mul_f32_e32 v14, 0x3b000000, v14
	v_pk_add_f32 v[6:7], v[6:7], v[14:15] op_sel_hi:[1,0] neg_lo:[0,1] neg_hi:[0,1]
	v_pk_add_f32 v[8:9], v[8:9], v[14:15] op_sel_hi:[1,0] neg_lo:[0,1] neg_hi:[0,1]
	v_pk_add_f32 v[10:11], v[10:11], v[14:15] op_sel_hi:[1,0] neg_lo:[0,1] neg_hi:[0,1]
	v_pk_add_f32 v[12:13], v[12:13], v[14:15] op_sel_hi:[1,0] neg_lo:[0,1] neg_hi:[0,1]
	v_pk_mul_f32 v[14:15], v[6:7], v[6:7]
	v_pk_mul_f32 v[16:17], v[8:9], v[8:9]
	v_add_f32_e32 v14, v14, v15
	v_add_f32_e32 v14, v14, v16
	v_pk_mul_f32 v[18:19], v[10:11], v[10:11]
	v_add_f32_e32 v14, v14, v17
	v_add_f32_e32 v14, v14, v18
	v_pk_mul_f32 v[20:21], v[12:13], v[12:13]
	v_add_f32_e32 v14, v14, v19
	v_add_f32_e32 v14, v14, v20
	v_add_f32_e32 v14, v14, v21
	s_waitcnt vmcnt(2)
	v_pk_mul_f32 v[10:11], v[0:1], v[10:11]
	v_pk_mul_f32 v[12:13], v[2:3], v[12:13]
	v_add_f32_dpp v14, v14, v14 quad_perm:[1,0,3,2] row_mask:0xf bank_mask:0xf bound_ctrl:1
	v_pk_mul_f32 v[6:7], v[32:33], v[6:7]
	v_pk_mul_f32 v[8:9], v[34:35], v[8:9]
	v_add_f32_dpp v14, v14, v14 quad_perm:[2,3,0,1] row_mask:0xf bank_mask:0xf bound_ctrl:1
	s_nop 1
	v_add_f32_dpp v14, v14, v14 row_half_mirror row_mask:0xf bank_mask:0xf bound_ctrl:1
	s_nop 1
	v_add_f32_dpp v14, v14, v14 row_mirror row_mask:0xf bank_mask:0xf bound_ctrl:1
	s_nop 0
	v_readlane_b32 s2, v14, 16
	v_readlane_b32 s3, v14, 48
	v_readlane_b32 s0, v14, 0
	v_readlane_b32 s1, v14, 32
	v_mov_b32_e32 v14, s2
	v_mov_b32_e32 v15, s3
	v_pk_add_f32 v[14:15], s[0:1], v[14:15]
	s_nop 0
	v_add_f32_e32 v14, v14, v15
	v_fmac_f32_e32 v51, 0x3b000000, v14
	v_mul_f32_e32 v14, 0x4f800000, v51
	v_cmp_gt_f32_e32 vcc, s5, v51
	s_nop 1
	v_cndmask_b32_e32 v14, v51, v14, vcc
	v_sqrt_f32_e32 v15, v14
	s_nop 0
	v_add_u32_e32 v0, -1, v15
	v_add_u32_e32 v1, 1, v15
	v_fma_f32 v16, -v0, v15, v14
	v_fma_f32 v17, -v1, v15, v14
	v_cmp_ge_f32_e64 s[0:1], 0, v16
	s_nop 1
	v_cndmask_b32_e64 v0, v15, v0, s[0:1]
	v_cmp_lt_f32_e64 s[0:1], 0, v17
	s_nop 1
	v_cndmask_b32_e64 v0, v0, v1, s[0:1]
	v_mul_f32_e32 v1, 0x37800000, v0
	v_cndmask_b32_e32 v0, v0, v1, vcc
	v_cmp_class_f32_e32 vcc, v14, v52
	s_nop 1
	v_cndmask_b32_e32 v0, v0, v14, vcc
	v_div_scale_f32 v1, s[0:1], v0, v0, 1.0
	v_rcp_f32_e32 v14, v1
	v_div_scale_f32 v2, vcc, 1.0, v0, 1.0
	v_fma_f32 v3, -v1, v14, 1.0
	v_fmac_f32_e32 v14, v3, v14
	v_mul_f32_e32 v3, v2, v14
	v_fma_f32 v15, -v1, v3, v2
	v_fmac_f32_e32 v3, v15, v14
	v_fma_f32 v1, -v1, v3, v2
	v_div_fmas_f32 v1, v1, v14, v3
	v_div_fixup_f32 v14, v1, v0, 1.0
	s_waitcnt vmcnt(1)
	v_pk_fma_f32 v[0:1], v[14:15], v[6:7], v[36:37] op_sel_hi:[0,1,1]
	v_pk_fma_f32 v[2:3], v[14:15], v[8:9], v[38:39] op_sel_hi:[0,1,1]
	s_waitcnt vmcnt(0)
	v_pk_fma_f32 v[6:7], v[14:15], v[10:11], v[40:41] op_sel_hi:[0,1,1]
	v_pk_fma_f32 v[8:9], v[14:15], v[12:13], v[42:43] op_sel_hi:[0,1,1]
	v_fma_mixlo_f16 v15, v0, s4, 0
	v_pk_mul_f32 v[10:11], v[2:3], s[4:5] op_sel_hi:[1,0]
	global_store_dwordx4 v[48:49], v[0:3], off sc1
	global_store_dwordx4 v[48:49], v[6:9], off offset:1024 sc1
	v_mul_f32_e32 v14, 0x43000000, v0
	v_fma_mixlo_f16 v17, v6, s4, 0
	v_pk_mul_f32 v[12:13], v[8:9], s[4:5] op_sel_hi:[1,0]
	v_fma_mixlo_f16 v0, v0, s4, -v15 op_sel_hi:[0,0,1]
	v_cvt_pk_f16_f32 v15, v10, v11
	v_mul_f32_e32 v16, 0x43000000, v6
	v_fma_mixlo_f16 v6, v6, s4, -v17 op_sel_hi:[0,0,1]
	v_cvt_pk_f16_f32 v17, v12, v13
	v_cvt_f32_f16_e32 v10, v15
	v_cvt_f32_f16_sdwa v11, v15 dst_sel:DWORD dst_unused:UNUSED_PAD src0_sel:WORD_1
	v_cvt_f32_f16_e32 v12, v17
	v_cvt_f32_f16_sdwa v13, v17 dst_sel:DWORD dst_unused:UNUSED_PAD src0_sel:WORD_1
	v_mul_f32_e32 v18, 0x43000000, v1
	v_fma_mixlo_f16 v19, v1, s4, 0
	v_pk_fma_f32 v[2:3], v[2:3], s[4:5], v[10:11] op_sel_hi:[1,0,1] neg_lo:[0,0,1] neg_hi:[0,0,1]
	v_mul_f32_e32 v20, 0x43000000, v7
	v_fma_mixlo_f16 v21, v7, s4, 0
	v_cvt_pk_f16_f32 v14, v14, v18
	v_fma_mixhi_f16 v0, v1, s4, -v19 op_sel_hi:[0,0,1]
	v_pk_fma_f32 v[8:9], v[8:9], s[4:5], v[12:13] op_sel_hi:[1,0,1] neg_lo:[0,0,1] neg_hi:[0,0,1]
	v_cvt_pk_f16_f32 v1, v2, v3
	v_lshl_add_u64 v[2:3], v[46:47], 0, v[4:5]
	v_cvt_pk_f16_f32 v16, v16, v20
	v_fma_mixhi_f16 v6, v7, s4, -v21 op_sel_hi:[0,0,1]
	global_store_dwordx2 v[44:45], v[14:15], off
	global_store_dwordx2 v[44:45], v[16:17], off offset:512
	v_cvt_pk_f16_f32 v7, v8, v9
	global_store_dwordx2 v[2:3], v[0:1], off
	global_store_dwordx2 v[2:3], v[6:7], off offset:512
	s_endpgm
	s_endpgm
	s_endpgm
	s_endpgm
	s_endpgm
	s_endpgm
	s_endpgm
	s_endpgm
	s_endpgm
	s_endpgm
	s_endpgm
	s_endpgm
	.section	.rodata,"a",@progbits
	.p2align	6, 0x0

_Z9ln_kernelILi0ELi2EEvPKflS1_S1_S1_S1_S1_S1_S1_PfPDF16_S3_iii:
	s_bitcmp1_b32 s2, 8
	s_cbranch_scc0 .Lprio_skip_q6
	s_setprio 1
.Lprio_skip_q6:
	s_load_dwordx4 s[12:15], s[0:1], 0x60
	s_load_dwordx2 s[16:17], s[0:1], 0x10
	s_load_dwordx4 s[8:11], s[0:1], 0x20
	v_lshrrev_b32_e32 v1, 6, v0
	v_lshl_or_b32 v2, s2, 2, v1
	s_waitcnt lgkmcnt(0)
	s_cmp_gt_i32 s13, -1
	v_ashrrev_i32_e32 v3, 31, v2
	s_cbranch_scc0 .LBB20_2
	s_ashr_i32 s2, s14, 31
	v_mov_b32_e32 v4, s14
	v_mov_b32_e32 v5, s2
	v_mad_u64_u32 v[4:5], s[2:3], s13, v2, v[4:5]
	v_mov_b32_e32 v6, v5
	v_mad_u64_u32 v[6:7], s[2:3], s13, v3, v[6:7]
	v_mov_b32_e32 v5, v6
	s_mov_b64 s[20:21], 0
	s_branch .LBB20_3

.LBB20_5:
	v_lshlrev_b32_e32 v0, 2, v0
	s_load_dwordx2 s[0:1], s[0:1], 0x8
	v_and_b32_e32 v54, 0xfc, v0
	v_lshlrev_b64 v[44:45], 11, v[2:3]
	v_lshlrev_b64 v[4:5], 11, v[4:5]
	s_waitcnt lgkmcnt(0)
	v_lshl_add_u64 v[24:25], s[18:19], 0, v[44:45]
	v_lshlrev_b32_e32 v0, 2, v54
	v_mov_b32_e32 v1, 0
	v_lshl_add_u64 v[4:5], s[14:15], 0, v[4:5]
	v_lshl_add_u64 v[20:21], v[4:5], 0, v[0:1]
	v_lshl_add_u64 v[26:27], v[24:25], 0, v[0:1]
	global_load_dwordx4 v[4:7], v[20:21], off
	global_load_dwordx4 v[8:11], v0, s[16:17]
	global_load_dwordx4 v[12:15], v0, s[16:17] offset:1024
	global_load_dwordx4 v[16:19], v[20:21], off offset:1024
	v_lshl_add_u64 v[28:29], s[0:1], 2, v[24:25]
	global_load_dwordx4 v[20:23], v[26:27], off
	v_lshl_add_u64 v[46:47], v[28:29], 0, v[0:1]
	global_load_dwordx4 v[24:27], v[26:27], off offset:1024
	s_nop 0
	global_load_dwordx4 v[28:31], v[46:47], off
	global_load_dwordx4 v[32:35], v[46:47], off offset:1024
	global_load_dwordx4 v[36:39], v0, s[8:9]
	global_load_dwordx4 v[40:43], v0, s[8:9] offset:1024
	v_lshl_add_u64 v[44:45], s[4:5], 0, v[44:45]
	v_lshl_add_u64 v[52:53], v[44:45], 0, v[0:1]
	global_load_dwordx4 v[44:47], v0, s[10:11]
	global_load_dwordx4 v[48:51], v0, s[10:11] offset:1024
	v_mov_b32_e32 v55, 0x3727c5ac
	s_mov_b32 s9, 0xf800000
	v_mov_b32_e32 v56, 0x260
	s_mov_b32 s8, 0x43000000
	v_lshlrev_b64 v[2:3], 10, v[2:3]
	s_waitcnt vmcnt(10)
	v_pk_add_f32 v[4:5], v[8:9], v[4:5]
	v_pk_add_f32 v[6:7], v[10:11], v[6:7]
	s_waitcnt vmcnt(8)
	v_pk_add_f32 v[8:9], v[12:13], v[16:17]
	v_pk_add_f32 v[10:11], v[14:15], v[18:19]
	s_waitcnt vmcnt(7)
	v_pk_add_f32 v[4:5], v[4:5], v[20:21]
	v_pk_add_f32 v[6:7], v[6:7], v[22:23]
	s_waitcnt vmcnt(5)
	v_pk_add_f32 v[4:5], v[4:5], v[28:29]
	v_pk_add_f32 v[6:7], v[6:7], v[30:31]
	v_add_f32_e32 v0, 0, v4
	v_add_f32_e32 v0, v0, v5
	v_pk_add_f32 v[8:9], v[8:9], v[24:25]
	v_add_f32_e32 v0, v0, v6
	s_waitcnt vmcnt(4)
	v_pk_add_f32 v[8:9], v[8:9], v[32:33]
	v_add_f32_e32 v0, v0, v7
	v_pk_add_f32 v[10:11], v[10:11], v[26:27]
	v_add_f32_e32 v0, v0, v8
	v_pk_add_f32 v[10:11], v[10:11], v[34:35]
	v_add_f32_e32 v0, v0, v9
	v_add_f32_e32 v0, v0, v10
	v_add_f32_e32 v0, v0, v11
	s_nop 1
	v_add_f32_dpp v0, v0, v0 quad_perm:[1,0,3,2] row_mask:0xf bank_mask:0xf bound_ctrl:1
	s_nop 1
	v_add_f32_dpp v0, v0, v0 quad_perm:[2,3,0,1] row_mask:0xf bank_mask:0xf bound_ctrl:1
	s_nop 1
	v_add_f32_dpp v0, v0, v0 row_half_mirror row_mask:0xf bank_mask:0xf bound_ctrl:1
	s_nop 1
	v_add_f32_dpp v0, v0, v0 row_mirror row_mask:0xf bank_mask:0xf bound_ctrl:1
	s_nop 0
	v_readlane_b32 s4, v0, 16
	v_readlane_b32 s5, v0, 48
	v_readlane_b32 s0, v0, 0
	v_readlane_b32 s1, v0, 32
	v_mov_b32_e32 v12, s4
	v_mov_b32_e32 v13, s5
	v_pk_add_f32 v[12:13], s[0:1], v[12:13]
	s_nop 0
	v_add_f32_e32 v0, v12, v13
	v_mul_f32_e32 v0, 0x3b000000, v0
	v_pk_add_f32 v[4:5], v[4:5], v[0:1] op_sel_hi:[1,0] neg_lo:[0,1] neg_hi:[0,1]
	v_pk_add_f32 v[6:7], v[6:7], v[0:1] op_sel_hi:[1,0] neg_lo:[0,1] neg_hi:[0,1]
	v_pk_mul_f32 v[12:13], v[4:5], v[4:5]
	v_pk_add_f32 v[8:9], v[8:9], v[0:1] op_sel_hi:[1,0] neg_lo:[0,1] neg_hi:[0,1]
	v_pk_add_f32 v[10:11], v[10:11], v[0:1] op_sel_hi:[1,0] neg_lo:[0,1] neg_hi:[0,1]
	v_pk_mul_f32 v[14:15], v[6:7], v[6:7]
	v_add_f32_e32 v0, v12, v13
	v_add_f32_e32 v0, v0, v14
	v_pk_mul_f32 v[16:17], v[8:9], v[8:9]
	v_add_f32_e32 v0, v0, v15
	v_add_f32_e32 v0, v0, v16
	v_pk_mul_f32 v[18:19], v[10:11], v[10:11]
	v_add_f32_e32 v0, v0, v17
	v_add_f32_e32 v0, v0, v18
	v_add_f32_e32 v0, v0, v19
	s_waitcnt vmcnt(3)
	v_pk_mul_f32 v[6:7], v[38:39], v[6:7]
	s_waitcnt vmcnt(2)
	v_pk_mul_f32 v[8:9], v[40:41], v[8:9]
	v_add_f32_dpp v0, v0, v0 quad_perm:[1,0,3,2] row_mask:0xf bank_mask:0xf bound_ctrl:1
	v_pk_mul_f32 v[4:5], v[36:37], v[4:5]
	v_pk_mul_f32 v[10:11], v[42:43], v[10:11]
	v_add_f32_dpp v0, v0, v0 quad_perm:[2,3,0,1] row_mask:0xf bank_mask:0xf bound_ctrl:1
	s_nop 1
	v_add_f32_dpp v0, v0, v0 row_half_mirror row_mask:0xf bank_mask:0xf bound_ctrl:1
	s_nop 1
	v_add_f32_dpp v0, v0, v0 row_mirror row_mask:0xf bank_mask:0xf bound_ctrl:1
	s_nop 0
	v_readlane_b32 s4, v0, 16
	v_readlane_b32 s5, v0, 48
	v_readlane_b32 s0, v0, 0
	v_readlane_b32 s1, v0, 32
	v_mov_b32_e32 v12, s4
	v_mov_b32_e32 v13, s5
	v_pk_add_f32 v[12:13], s[0:1], v[12:13]
	s_nop 0
	v_add_f32_e32 v0, v12, v13
	v_fmac_f32_e32 v55, 0x3b000000, v0
	v_mul_f32_e32 v0, 0x4f800000, v55
	v_cmp_gt_f32_e32 vcc, s9, v55
	s_nop 1
	v_cndmask_b32_e32 v0, v55, v0, vcc
	v_sqrt_f32_e32 v12, v0
	s_nop 0
	v_add_u32_e32 v13, -1, v12
	v_add_u32_e32 v14, 1, v12
	v_fma_f32 v15, -v13, v12, v0
	v_fma_f32 v16, -v14, v12, v0
	v_cmp_ge_f32_e64 s[0:1], 0, v15
	s_nop 1
	v_cndmask_b32_e64 v12, v12, v13, s[0:1]
	v_cmp_lt_f32_e64 s[0:1], 0, v16
	s_nop 1
	v_cndmask_b32_e64 v12, v12, v14, s[0:1]
	v_mul_f32_e32 v13, 0x37800000, v12
	v_cndmask_b32_e32 v12, v12, v13, vcc
	v_cmp_class_f32_e32 vcc, v0, v56
	s_nop 1
	v_cndmask_b32_e32 v0, v12, v0, vcc
	v_div_scale_f32 v12, s[0:1], v0, v0, 1.0
	v_rcp_f32_e32 v13, v12
	v_div_scale_f32 v14, vcc, 1.0, v0, 1.0
	v_fma_f32 v15, -v12, v13, 1.0
	v_fmac_f32_e32 v13, v15, v13
	v_mul_f32_e32 v15, v14, v13
	v_fma_f32 v16, -v12, v15, v14
	v_fmac_f32_e32 v15, v16, v13
	v_fma_f32 v12, -v12, v15, v14
	v_div_fmas_f32 v12, v12, v13, v15
	v_div_fixup_f32 v0, v12, v0, 1.0
	s_waitcnt vmcnt(1)
	v_pk_fma_f32 v[6:7], v[0:1], v[6:7], v[46:47] op_sel_hi:[0,1,1]
	s_waitcnt vmcnt(0)
	v_pk_fma_f32 v[8:9], v[0:1], v[8:9], v[48:49] op_sel_hi:[0,1,1]
	v_pk_fma_f32 v[4:5], v[0:1], v[4:5], v[44:45] op_sel_hi:[0,1,1]
	v_mul_f32_e32 v17, 0x43000000, v8
	v_fma_mixlo_f16 v18, v8, s8, 0
	v_mul_f32_e32 v21, 0x43000000, v9
	v_pk_mul_f32 v[12:13], v[6:7], s[8:9] op_sel_hi:[1,0]
	v_pk_fma_f32 v[10:11], v[0:1], v[10:11], v[50:51] op_sel_hi:[0,1,1]
	global_store_dwordx4 v[52:53], v[4:7], off sc1
	global_store_dwordx4 v[52:53], v[8:11], off offset:1024 sc1
	v_mul_f32_e32 v0, 0x43000000, v4
	v_fma_mixlo_f16 v16, v4, s8, 0
	v_fma_mixlo_f16 v8, v8, s8, -v18 op_sel_hi:[0,0,1]
	v_cvt_pk_f16_f32 v18, v17, v21
	v_cvt_pk_f16_f32 v17, v12, v13
	v_mul_f32_e32 v19, 0x43000000, v5
	v_pk_mul_f32 v[14:15], v[10:11], s[8:9] op_sel_hi:[1,0]
	v_cvt_f32_f16_e32 v12, v17
	v_cvt_f32_f16_sdwa v13, v17 dst_sel:DWORD dst_unused:UNUSED_PAD src0_sel:WORD_1
	v_fma_mixlo_f16 v4, v4, s8, -v16 op_sel_hi:[0,0,1]
	v_cvt_pk_f16_f32 v16, v0, v19
	v_cvt_pk_f16_f32 v19, v14, v15
	v_cvt_f32_f16_e32 v14, v19
	v_cvt_f32_f16_sdwa v15, v19 dst_sel:DWORD dst_unused:UNUSED_PAD src0_sel:WORD_1
	v_fma_mixlo_f16 v20, v5, s8, 0
	v_pk_fma_f32 v[6:7], v[6:7], s[8:9], v[12:13] op_sel_hi:[1,0,1] neg_lo:[0,0,1] neg_hi:[0,0,1]
	v_fma_mixhi_f16 v4, v5, s8, -v20 op_sel_hi:[0,0,1]
	v_cvt_pk_f16_f32 v5, v6, v7
	v_lshl_add_u64 v[6:7], s[6:7], 0, v[2:3]
	v_lshlrev_b32_e32 v0, 1, v54
	v_lshl_add_u64 v[2:3], s[2:3], 0, v[2:3]
	v_fma_mixlo_f16 v22, v9, s8, 0
	v_pk_fma_f32 v[10:11], v[10:11], s[8:9], v[14:15] op_sel_hi:[1,0,1] neg_lo:[0,0,1] neg_hi:[0,0,1]
	v_lshl_add_u64 v[6:7], v[6:7], 0, v[0:1]
	v_lshl_add_u64 v[0:1], v[2:3], 0, v[0:1]
	v_fma_mixhi_f16 v8, v9, s8, -v22 op_sel_hi:[0,0,1]
	v_cvt_pk_f16_f32 v9, v10, v11
	global_store_dwordx2 v[6:7], v[16:17], off
	global_store_dwordx2 v[6:7], v[18:19], off offset:512
	global_store_dwordx2 v[0:1], v[4:5], off
	global_store_dwordx2 v[0:1], v[8:9], off offset:512
	s_endpgm
	s_endpgm
	s_endpgm
	s_endpgm
	s_endpgm
	s_endpgm
	s_endpgm
	s_endpgm
	s_endpgm
	s_endpgm
	s_endpgm
	s_endpgm
	s_endpgm
	s_endpgm
	s_endpgm
	s_endpgm
	s_endpgm
	s_endpgm
	s_endpgm
	s_endpgm
	s_endpgm
	s_endpgm
	s_endpgm
	s_endpgm
	s_endpgm
	s_endpgm
	s_endpgm
	s_endpgm
	s_endpgm
	s_endpgm
	s_endpgm
	s_endpgm
	s_endpgm
	s_endpgm
	s_endpgm
	s_endpgm
	s_endpgm
	s_endpgm
	s_endpgm
	s_endpgm
	s_endpgm
	s_endpgm
	s_endpgm
	s_endpgm
	s_endpgm
	s_endpgm
	s_endpgm
	s_endpgm
	s_endpgm
	s_endpgm
	s_endpgm
	s_endpgm
	s_endpgm
	s_endpgm
	.section	.rodata,"a",@progbits
	.p2align	6, 0x0

_Z9ln_kernelILi0ELi4EEvPKflS1_S1_S1_S1_S1_S1_S1_PfPDF16_S3_iii:
	s_bitcmp1_b32 s2, 8
	s_cbranch_scc0 .Lprio_skip_q7
	s_setprio 1

.LBB21_5:
	v_lshlrev_b32_e32 v0, 2, v0
	v_and_b32_e32 v58, 0xfc, v0
	v_lshlrev_b64 v[4:5], 11, v[4:5]
	v_lshlrev_b32_e32 v0, 2, v58
	v_mov_b32_e32 v1, 0
	s_waitcnt lgkmcnt(0)
	v_lshl_add_u64 v[4:5], s[18:19], 0, v[4:5]
	v_lshl_add_u64 v[20:21], v[4:5], 0, v[0:1]
	global_load_dwordx4 v[4:7], v[20:21], off
	global_load_dwordx4 v[8:11], v0, s[16:17]
	global_load_dwordx4 v[12:15], v0, s[16:17] offset:1024
	global_load_dwordx4 v[16:19], v[20:21], off offset:1024
	s_load_dwordx2 s[0:1], s[0:1], 0x8
	v_lshlrev_b64 v[52:53], 11, v[2:3]
	v_lshl_add_u64 v[28:29], s[14:15], 0, v[52:53]
	v_lshl_add_u64 v[24:25], v[28:29], 0, v[0:1]
	v_mov_b32_e32 v59, 0x3727c5ac
	s_waitcnt lgkmcnt(0)
	v_lshl_add_u64 v[20:21], s[0:1], 2, v[28:29]
	v_lshl_add_u64 v[26:27], s[0:1], 3, v[28:29]
	v_lshl_add_u64 v[36:37], v[20:21], 0, v[0:1]
	global_load_dwordx4 v[20:23], v[24:25], off
	v_lshl_add_u64 v[40:41], v[26:27], 0, v[0:1]
	global_load_dwordx4 v[24:27], v[24:25], off offset:1024
	v_mad_u64_u32 v[44:45], s[12:13], s0, 12, v[28:29]
	v_mov_b32_e32 v38, v45
	v_mad_u64_u32 v[42:43], s[0:1], s1, 12, v[38:39]
	global_load_dwordx4 v[28:31], v[36:37], off
	global_load_dwordx4 v[32:35], v[36:37], off offset:1024
	v_mov_b32_e32 v45, v42
	global_load_dwordx4 v[36:39], v[40:41], off
	v_lshl_add_u64 v[54:55], v[44:45], 0, v[0:1]
	global_load_dwordx4 v[40:43], v[40:41], off offset:1024
	s_nop 0
	global_load_dwordx4 v[44:47], v[54:55], off
	global_load_dwordx4 v[48:51], v[54:55], off offset:1024
	v_mov_b32_e32 v60, 0x260
	v_lshlrev_b64 v[2:3], 10, v[2:3]
	s_waitcnt vmcnt(10)
	v_pk_add_f32 v[54:55], v[8:9], v[4:5]
	v_pk_add_f32 v[56:57], v[10:11], v[6:7]
	global_load_dwordx4 v[4:7], v0, s[8:9]
	global_load_dwordx4 v[8:11], v0, s[8:9] offset:1024
	s_waitcnt vmcnt(10)
	v_pk_add_f32 v[16:17], v[12:13], v[16:17]
	v_lshl_add_u64 v[12:13], s[4:5], 0, v[52:53]
	v_pk_add_f32 v[18:19], v[14:15], v[18:19]
	v_lshl_add_u64 v[52:53], v[12:13], 0, v[0:1]
	global_load_dwordx4 v[12:15], v0, s[10:11]
	s_mov_b32 s9, 0xf800000
	s_mov_b32 s8, 0x43000000
	s_waitcnt vmcnt(10)
	v_pk_add_f32 v[20:21], v[54:55], v[20:21]
	v_pk_add_f32 v[22:23], v[56:57], v[22:23]
	s_waitcnt vmcnt(9)
	v_pk_add_f32 v[24:25], v[16:17], v[24:25]
	v_pk_add_f32 v[26:27], v[18:19], v[26:27]
	global_load_dwordx4 v[16:19], v0, s[10:11] offset:1024
	s_waitcnt vmcnt(9)
	v_pk_add_f32 v[20:21], v[20:21], v[28:29]
	v_pk_add_f32 v[22:23], v[22:23], v[30:31]
	s_waitcnt vmcnt(8)
	v_pk_add_f32 v[24:25], v[24:25], v[32:33]
	s_waitcnt vmcnt(7)
	v_pk_add_f32 v[20:21], v[20:21], v[36:37]
	v_pk_add_f32 v[22:23], v[22:23], v[38:39]
	s_waitcnt vmcnt(5)
	v_pk_add_f32 v[20:21], v[20:21], v[44:45]
	v_pk_add_f32 v[22:23], v[22:23], v[46:47]
	v_add_f32_e32 v0, 0, v20
	v_add_f32_e32 v0, v0, v21
	v_pk_add_f32 v[24:25], v[24:25], v[40:41]
	v_add_f32_e32 v0, v0, v22
	v_pk_add_f32 v[26:27], v[26:27], v[34:35]
	s_waitcnt vmcnt(4)
	v_pk_add_f32 v[24:25], v[24:25], v[48:49]
	v_add_f32_e32 v0, v0, v23
	v_pk_add_f32 v[26:27], v[26:27], v[42:43]
	v_add_f32_e32 v0, v0, v24
	v_pk_add_f32 v[26:27], v[26:27], v[50:51]
	v_add_f32_e32 v0, v0, v25
	v_add_f32_e32 v0, v0, v26
	v_add_f32_e32 v0, v0, v27
	s_nop 1
	v_add_f32_dpp v0, v0, v0 quad_perm:[1,0,3,2] row_mask:0xf bank_mask:0xf bound_ctrl:1
	s_nop 1
	v_add_f32_dpp v0, v0, v0 quad_perm:[2,3,0,1] row_mask:0xf bank_mask:0xf bound_ctrl:1
	s_nop 1
	v_add_f32_dpp v0, v0, v0 row_half_mirror row_mask:0xf bank_mask:0xf bound_ctrl:1
	s_nop 1
	v_add_f32_dpp v0, v0, v0 row_mirror row_mask:0xf bank_mask:0xf bound_ctrl:1
	s_nop 0
	v_readlane_b32 s4, v0, 16
	v_readlane_b32 s5, v0, 48
	v_readlane_b32 s0, v0, 0
	v_readlane_b32 s1, v0, 32
	v_mov_b32_e32 v28, s4
	v_mov_b32_e32 v29, s5
	v_pk_add_f32 v[28:29], s[0:1], v[28:29]
	s_nop 0
	v_add_f32_e32 v0, v28, v29
	v_mul_f32_e32 v0, 0x3b000000, v0
	v_pk_add_f32 v[20:21], v[20:21], v[0:1] op_sel_hi:[1,0] neg_lo:[0,1] neg_hi:[0,1]
	v_pk_add_f32 v[22:23], v[22:23], v[0:1] op_sel_hi:[1,0] neg_lo:[0,1] neg_hi:[0,1]
	v_pk_mul_f32 v[28:29], v[20:21], v[20:21]
	v_pk_add_f32 v[24:25], v[24:25], v[0:1] op_sel_hi:[1,0] neg_lo:[0,1] neg_hi:[0,1]
	v_pk_add_f32 v[26:27], v[26:27], v[0:1] op_sel_hi:[1,0] neg_lo:[0,1] neg_hi:[0,1]
	v_pk_mul_f32 v[30:31], v[22:23], v[22:23]
	v_add_f32_e32 v0, v28, v29
	v_add_f32_e32 v0, v0, v30
	v_pk_mul_f32 v[32:33], v[24:25], v[24:25]
	v_add_f32_e32 v0, v0, v31
	v_add_f32_e32 v0, v0, v32
	v_pk_mul_f32 v[34:35], v[26:27], v[26:27]
	v_add_f32_e32 v0, v0, v33
	v_add_f32_e32 v0, v0, v34
	v_add_f32_e32 v0, v0, v35
	s_waitcnt vmcnt(3)
	v_pk_mul_f32 v[4:5], v[4:5], v[20:21]
	v_add_f32_dpp v0, v0, v0 quad_perm:[1,0,3,2] row_mask:0xf bank_mask:0xf bound_ctrl:1
	v_pk_mul_f32 v[6:7], v[6:7], v[22:23]
	s_waitcnt vmcnt(2)
	v_pk_mul_f32 v[8:9], v[8:9], v[24:25]
	v_add_f32_dpp v0, v0, v0 quad_perm:[2,3,0,1] row_mask:0xf bank_mask:0xf bound_ctrl:1
	v_pk_mul_f32 v[10:11], v[10:11], v[26:27]
	s_nop 0
	v_add_f32_dpp v0, v0, v0 row_half_mirror row_mask:0xf bank_mask:0xf bound_ctrl:1
	s_nop 1
	v_add_f32_dpp v0, v0, v0 row_mirror row_mask:0xf bank_mask:0xf bound_ctrl:1
	s_nop 0
	v_readlane_b32 s4, v0, 16
	v_readlane_b32 s5, v0, 48
	v_readlane_b32 s0, v0, 0
	v_readlane_b32 s1, v0, 32
	v_mov_b32_e32 v28, s4
	v_mov_b32_e32 v29, s5
	v_pk_add_f32 v[28:29], s[0:1], v[28:29]
	s_nop 0
	v_add_f32_e32 v0, v28, v29
	v_fmac_f32_e32 v59, 0x3b000000, v0
	v_mul_f32_e32 v0, 0x4f800000, v59
	v_cmp_gt_f32_e32 vcc, s9, v59
	s_nop 1
	v_cndmask_b32_e32 v0, v59, v0, vcc
	v_sqrt_f32_e32 v28, v0
	s_nop 0
	v_add_u32_e32 v20, -1, v28
	v_add_u32_e32 v21, 1, v28
	v_fma_f32 v22, -v20, v28, v0
	v_fma_f32 v23, -v21, v28, v0
	v_cmp_ge_f32_e64 s[0:1], 0, v22
	s_nop 1
	v_cndmask_b32_e64 v20, v28, v20, s[0:1]
	v_cmp_lt_f32_e64 s[0:1], 0, v23
	s_nop 1
	v_cndmask_b32_e64 v20, v20, v21, s[0:1]
	v_mul_f32_e32 v21, 0x37800000, v20
	v_cndmask_b32_e32 v20, v20, v21, vcc
	v_cmp_class_f32_e32 vcc, v0, v60
	s_nop 1
	v_cndmask_b32_e32 v0, v20, v0, vcc
	v_div_scale_f32 v20, s[0:1], v0, v0, 1.0
	v_rcp_f32_e32 v21, v20
	v_div_scale_f32 v22, vcc, 1.0, v0, 1.0
	v_fma_f32 v23, -v20, v21, 1.0
	v_fmac_f32_e32 v21, v23, v21
	v_mul_f32_e32 v23, v22, v21
	v_fma_f32 v24, -v20, v23, v22
	v_fmac_f32_e32 v23, v24, v21
	v_fma_f32 v20, -v20, v23, v22
	v_div_fmas_f32 v20, v20, v21, v23
	v_div_fixup_f32 v0, v20, v0, 1.0
	s_waitcnt vmcnt(1)
	v_pk_fma_f32 v[4:5], v[0:1], v[4:5], v[12:13] op_sel_hi:[0,1,1]
	v_pk_fma_f32 v[6:7], v[0:1], v[6:7], v[14:15] op_sel_hi:[0,1,1]
	s_waitcnt vmcnt(0)
	v_pk_fma_f32 v[8:9], v[0:1], v[8:9], v[16:17] op_sel_hi:[0,1,1]
	v_fma_mixlo_f16 v12, v4, s8, 0
	v_pk_fma_f32 v[10:11], v[0:1], v[10:11], v[18:19] op_sel_hi:[0,1,1]
	global_store_dwordx4 v[52:53], v[4:7], off sc1
	global_store_dwordx4 v[52:53], v[8:11], off offset:1024 sc1
	v_mul_f32_e32 v0, 0x43000000, v4
	v_fma_mixlo_f16 v4, v4, s8, -v12 op_sel_hi:[0,0,1]
	v_fma_mixlo_f16 v12, v8, s8, 0
	v_mul_f32_e32 v13, 0x43000000, v8
	v_fma_mixlo_f16 v8, v8, s8, -v12 op_sel_hi:[0,0,1]
	v_mul_f32_e32 v12, 0x43000000, v5
	v_fma_mixlo_f16 v14, v5, s8, 0
	v_cvt_pk_f16_f32 v12, v0, v12
	v_mul_f32_e32 v0, 0x43000000, v9
	v_pk_mul_f32 v[16:17], v[6:7], s[8:9] op_sel_hi:[1,0]
	v_fma_mixhi_f16 v4, v5, s8, -v14 op_sel_hi:[0,0,1]
	v_cvt_pk_f16_f32 v14, v13, v0
	v_cvt_pk_f16_f32 v13, v16, v17
	v_pk_mul_f32 v[18:19], v[10:11], s[8:9] op_sel_hi:[1,0]
	v_cvt_f32_f16_e32 v16, v13
	v_cvt_f32_f16_sdwa v17, v13 dst_sel:DWORD dst_unused:UNUSED_PAD src0_sel:WORD_1
	v_cvt_pk_f16_f32 v15, v18, v19
	v_cvt_f32_f16_e32 v18, v15
	v_cvt_f32_f16_sdwa v19, v15 dst_sel:DWORD dst_unused:UNUSED_PAD src0_sel:WORD_1
	v_fma_mixlo_f16 v5, v9, s8, 0
	v_pk_fma_f32 v[6:7], v[6:7], s[8:9], v[16:17] op_sel_hi:[1,0,1] neg_lo:[0,0,1] neg_hi:[0,0,1]
	v_fma_mixhi_f16 v8, v9, s8, -v5 op_sel_hi:[0,0,1]
	v_cvt_pk_f16_f32 v5, v6, v7
	v_pk_fma_f32 v[6:7], v[10:11], s[8:9], v[18:19] op_sel_hi:[1,0,1] neg_lo:[0,0,1] neg_hi:[0,0,1]
	v_lshlrev_b32_e32 v0, 1, v58
	v_cvt_pk_f16_f32 v9, v6, v7
	v_lshl_add_u64 v[6:7], s[6:7], 0, v[2:3]
	v_lshl_add_u64 v[2:3], s[2:3], 0, v[2:3]
	v_lshl_add_u64 v[6:7], v[6:7], 0, v[0:1]
	v_lshl_add_u64 v[0:1], v[2:3], 0, v[0:1]
	global_store_dwordx2 v[6:7], v[12:13], off
	global_store_dwordx2 v[6:7], v[14:15], off offset:512
	global_store_dwordx2 v[0:1], v[4:5], off
	global_store_dwordx2 v[0:1], v[8:9], off offset:512
	s_endpgm
	s_endpgm
	s_endpgm
	s_endpgm
	s_endpgm
	s_endpgm
	s_endpgm
	s_endpgm
	s_endpgm
	s_endpgm
	s_endpgm
	s_endpgm
	s_endpgm
	.section	.rodata,"a",@progbits
	.p2align	6, 0x0

_Z9ln_kernelILi0ELi8EEvPKflS1_S1_S1_S1_S1_S1_S1_PfPDF16_S3_iii:
	s_bitcmp1_b32 s2, 8
	s_cbranch_scc0 .Lprio_skip_q8
	s_setprio 1

.LBB22_5:
	v_lshlrev_b32_e32 v0, 2, v0
	v_and_b32_e32 v66, 0xfc, v0
	v_lshlrev_b64 v[4:5], 11, v[4:5]
	v_lshlrev_b32_e32 v0, 2, v66
	v_mov_b32_e32 v1, 0
	s_waitcnt lgkmcnt(0)
	v_lshl_add_u64 v[4:5], s[18:19], 0, v[4:5]
	v_lshl_add_u64 v[20:21], v[4:5], 0, v[0:1]
	global_load_dwordx4 v[4:7], v[20:21], off
	global_load_dwordx4 v[8:11], v0, s[16:17]
	global_load_dwordx4 v[12:15], v0, s[16:17] offset:1024
	global_load_dwordx4 v[16:19], v[20:21], off offset:1024
	v_lshlrev_b64 v[48:49], 11, v[2:3]
	v_lshl_add_u64 v[40:41], s[14:15], 0, v[48:49]
	v_lshl_add_u64 v[28:29], v[40:41], 0, v[0:1]
	global_load_dwordx4 v[20:23], v[28:29], off
	global_load_dwordx4 v[24:27], v[28:29], off offset:1024
	s_load_dwordx2 s[0:1], s[0:1], 0x8
	v_lshlrev_b64 v[2:3], 10, v[2:3]
	s_waitcnt lgkmcnt(0)
	v_lshl_add_u64 v[28:29], s[0:1], 2, v[40:41]
	v_lshl_add_u64 v[42:43], v[28:29], 0, v[0:1]
	v_mad_u64_u32 v[36:37], s[12:13], s0, 12, v[40:41]
	v_lshl_add_u64 v[32:33], s[0:1], 3, v[40:41]
	global_load_dwordx4 v[28:31], v[42:43], off
	v_mov_b32_e32 v38, v37
	v_lshl_add_u64 v[44:45], v[32:33], 0, v[0:1]
	v_mad_u64_u32 v[38:39], s[12:13], s1, 12, v[38:39]
	global_load_dwordx4 v[32:35], v[44:45], off
	v_mov_b32_e32 v37, v38
	v_lshl_add_u64 v[46:47], v[36:37], 0, v[0:1]
	global_load_dwordx4 v[36:39], v[46:47], off
	v_mad_u64_u32 v[52:53], s[12:13], s0, 20, v[40:41]
	v_mad_u64_u32 v[54:55], s[12:13], s0, 24, v[40:41]
	v_lshl_add_u64 v[50:51], s[0:1], 4, v[40:41]
	v_mad_u64_u32 v[40:41], s[12:13], s0, 28, v[40:41]
	v_lshl_add_u64 v[50:51], v[50:51], 0, v[0:1]
	s_waitcnt vmcnt(7)
	v_pk_add_f32 v[56:57], v[8:9], v[4:5]
	v_mov_b32_e32 v4, v53
	v_pk_add_f32 v[58:59], v[10:11], v[6:7]
	v_mov_b32_e32 v6, v55
	v_mad_u64_u32 v[10:11], s[12:13], s1, 20, v[4:5]
	s_waitcnt vmcnt(5)
	v_pk_add_f32 v[60:61], v[12:13], v[16:17]
	v_mov_b32_e32 v8, v41
	v_mad_u64_u32 v[12:13], s[12:13], s1, 24, v[6:7]
	v_mov_b32_e32 v53, v10
	v_pk_add_f32 v[62:63], v[14:15], v[18:19]
	v_mad_u64_u32 v[14:15], s[0:1], s1, 28, v[8:9]
	global_load_dwordx4 v[4:7], v[50:51], off
	v_mov_b32_e32 v55, v12
	v_lshl_add_u64 v[52:53], v[52:53], 0, v[0:1]
	v_mov_b32_e32 v41, v14
	v_lshl_add_u64 v[54:55], v[54:55], 0, v[0:1]
	global_load_dwordx4 v[12:15], v[52:53], off
	v_lshl_add_u64 v[64:65], v[40:41], 0, v[0:1]
	global_load_dwordx4 v[16:19], v[54:55], off
	global_load_dwordx4 v[8:11], v[42:43], off offset:1024
	s_waitcnt vmcnt(8)
	v_pk_add_f32 v[40:41], v[56:57], v[20:21]
	v_pk_add_f32 v[42:43], v[58:59], v[22:23]
	global_load_dwordx4 v[20:23], v[64:65], off
	s_waitcnt vmcnt(8)
	v_pk_add_f32 v[56:57], v[60:61], v[24:25]
	v_pk_add_f32 v[58:59], v[62:63], v[26:27]
	s_waitcnt vmcnt(7)
	v_pk_add_f32 v[40:41], v[40:41], v[28:29]
	v_pk_add_f32 v[42:43], v[42:43], v[30:31]
	global_load_dwordx4 v[24:27], v[44:45], off offset:1024
	global_load_dwordx4 v[28:31], v[46:47], off offset:1024
	s_waitcnt vmcnt(8)
	v_pk_add_f32 v[44:45], v[40:41], v[32:33]
	v_pk_add_f32 v[46:47], v[42:43], v[34:35]
	global_load_dwordx4 v[32:35], v[50:51], off offset:1024
	global_load_dwordx4 v[40:43], v[52:53], off offset:1024
	s_waitcnt vmcnt(9)
	v_pk_add_f32 v[50:51], v[44:45], v[36:37]
	v_pk_add_f32 v[52:53], v[46:47], v[38:39]
	global_load_dwordx4 v[36:39], v[54:55], off offset:1024
	global_load_dwordx4 v[44:47], v[64:65], off offset:1024
	s_waitcnt vmcnt(10)
	v_pk_add_f32 v[4:5], v[50:51], v[4:5]
	v_pk_add_f32 v[6:7], v[52:53], v[6:7]
	s_waitcnt vmcnt(9)
	v_pk_add_f32 v[50:51], v[4:5], v[12:13]
	v_pk_add_f32 v[52:53], v[6:7], v[14:15]
	global_load_dwordx4 v[4:7], v0, s[8:9]
	global_load_dwordx4 v[12:15], v0, s[10:11]
	s_waitcnt vmcnt(10)
	v_pk_add_f32 v[16:17], v[50:51], v[16:17]
	v_pk_add_f32 v[18:19], v[52:53], v[18:19]
	s_waitcnt vmcnt(9)
	v_pk_add_f32 v[8:9], v[56:57], v[8:9]
	s_waitcnt vmcnt(8)
	v_pk_add_f32 v[50:51], v[16:17], v[20:21]
	v_pk_add_f32 v[52:53], v[18:19], v[22:23]
	global_load_dwordx4 v[16:19], v0, s[8:9] offset:1024
	global_load_dwordx4 v[20:23], v0, s[10:11] offset:1024
	v_pk_add_f32 v[10:11], v[58:59], v[10:11]
	s_waitcnt vmcnt(9)
	v_pk_add_f32 v[8:9], v[8:9], v[24:25]
	v_add_f32_e32 v24, 0, v50
	s_waitcnt vmcnt(8)
	v_pk_add_f32 v[8:9], v[8:9], v[28:29]
	v_pk_add_f32 v[10:11], v[10:11], v[26:27]
	s_waitcnt vmcnt(7)
	v_pk_add_f32 v[8:9], v[8:9], v[32:33]
	v_add_f32_e32 v24, v24, v51
	s_waitcnt vmcnt(6)
	v_pk_add_f32 v[8:9], v[8:9], v[40:41]
	v_pk_add_f32 v[10:11], v[10:11], v[30:31]
	v_add_f32_e32 v24, v24, v52
	s_waitcnt vmcnt(5)
	v_pk_add_f32 v[8:9], v[8:9], v[36:37]
	v_pk_add_f32 v[10:11], v[10:11], v[34:35]
	v_add_f32_e32 v24, v24, v53
	s_waitcnt vmcnt(4)
	v_pk_add_f32 v[8:9], v[8:9], v[44:45]
	v_pk_add_f32 v[10:11], v[10:11], v[42:43]
	v_add_f32_e32 v24, v24, v8
	v_pk_add_f32 v[10:11], v[10:11], v[38:39]
	v_add_f32_e32 v24, v24, v9
	v_pk_add_f32 v[10:11], v[10:11], v[46:47]
	s_nop 0
	v_add_f32_e32 v24, v24, v10
	v_add_f32_e32 v24, v24, v11
	s_nop 1
	v_add_f32_dpp v24, v24, v24 quad_perm:[1,0,3,2] row_mask:0xf bank_mask:0xf bound_ctrl:1
	s_nop 1
	v_add_f32_dpp v24, v24, v24 quad_perm:[2,3,0,1] row_mask:0xf bank_mask:0xf bound_ctrl:1
	s_nop 1
	v_add_f32_dpp v24, v24, v24 row_half_mirror row_mask:0xf bank_mask:0xf bound_ctrl:1
	s_nop 1
	v_add_f32_dpp v24, v24, v24 row_mirror row_mask:0xf bank_mask:0xf bound_ctrl:1
	s_nop 0
	v_readlane_b32 s8, v24, 16
	v_readlane_b32 s9, v24, 48
	v_readlane_b32 s0, v24, 0
	v_readlane_b32 s1, v24, 32
	v_mov_b32_e32 v24, s8
	v_mov_b32_e32 v25, s9
	v_pk_add_f32 v[24:25], s[0:1], v[24:25]
	s_nop 0
	v_add_f32_e32 v24, v24, v25
	v_mul_f32_e32 v24, 0x3b000000, v24
	v_pk_add_f32 v[26:27], v[50:51], v[24:25] op_sel_hi:[1,0] neg_lo:[0,1] neg_hi:[0,1]
	v_pk_add_f32 v[30:31], v[52:53], v[24:25] op_sel_hi:[1,0] neg_lo:[0,1] neg_hi:[0,1]
	v_pk_mul_f32 v[28:29], v[26:27], v[26:27]
	v_pk_mul_f32 v[32:33], v[30:31], v[30:31]
	v_add_f32_e32 v28, v28, v29
	v_pk_add_f32 v[8:9], v[8:9], v[24:25] op_sel_hi:[1,0] neg_lo:[0,1] neg_hi:[0,1]
	v_add_f32_e32 v28, v28, v32
	v_pk_mul_f32 v[34:35], v[8:9], v[8:9]
	v_add_f32_e32 v28, v28, v33
	v_pk_add_f32 v[10:11], v[10:11], v[24:25] op_sel_hi:[1,0] neg_lo:[0,1] neg_hi:[0,1]
	v_add_f32_e32 v28, v28, v34
	v_pk_mul_f32 v[24:25], v[10:11], v[10:11]
	v_add_f32_e32 v28, v28, v35
	v_add_f32_e32 v24, v28, v24
	v_add_f32_e32 v24, v24, v25
	s_waitcnt vmcnt(3)
	v_pk_mul_f32 v[4:5], v[4:5], v[26:27]
	v_add_f32_dpp v24, v24, v24 quad_perm:[1,0,3,2] row_mask:0xf bank_mask:0xf bound_ctrl:1
	v_pk_mul_f32 v[6:7], v[6:7], v[30:31]
	s_waitcnt vmcnt(1)
	v_pk_mul_f32 v[8:9], v[16:17], v[8:9]
	v_add_f32_dpp v24, v24, v24 quad_perm:[2,3,0,1] row_mask:0xf bank_mask:0xf bound_ctrl:1
	v_pk_mul_f32 v[10:11], v[18:19], v[10:11]
	s_nop 0
	v_add_f32_dpp v24, v24, v24 row_half_mirror row_mask:0xf bank_mask:0xf bound_ctrl:1
	s_nop 1
	v_add_f32_dpp v24, v24, v24 row_mirror row_mask:0xf bank_mask:0xf bound_ctrl:1
	s_nop 0
	v_readlane_b32 s8, v24, 16
	v_readlane_b32 s9, v24, 48
	v_readlane_b32 s0, v24, 0
	v_readlane_b32 s1, v24, 32
	v_mov_b32_e32 v24, s8
	v_mov_b32_e32 v25, s9
	v_pk_add_f32 v[24:25], s[0:1], v[24:25]
	s_mov_b32 s0, 0xf800000
	v_add_f32_e32 v24, v24, v25
	v_mov_b32_e32 v25, 0x3727c5ac
	v_fmac_f32_e32 v25, 0x3b000000, v24
	v_mul_f32_e32 v24, 0x4f800000, v25
	v_cmp_gt_f32_e32 vcc, s0, v25
	s_nop 1
	v_cndmask_b32_e32 v24, v25, v24, vcc
	v_sqrt_f32_e32 v25, v24
	s_nop 0
	v_add_u32_e32 v28, -1, v25
	v_fma_f32 v29, -v28, v25, v24
	v_cmp_ge_f32_e64 s[0:1], 0, v29
	v_add_u32_e32 v29, 1, v25
	s_nop 0
	v_cndmask_b32_e64 v28, v25, v28, s[0:1]
	v_fma_f32 v25, -v29, v25, v24
	v_cmp_lt_f32_e64 s[0:1], 0, v25
	s_nop 1
	v_cndmask_b32_e64 v25, v28, v29, s[0:1]
	v_mul_f32_e32 v28, 0x37800000, v25
	v_cndmask_b32_e32 v25, v25, v28, vcc
	v_mov_b32_e32 v28, 0x260
	v_cmp_class_f32_e32 vcc, v24, v28
	s_nop 1
	v_cndmask_b32_e32 v28, v25, v24, vcc
	v_div_scale_f32 v29, s[0:1], v28, v28, 1.0
	v_rcp_f32_e32 v32, v29
	v_lshl_add_u64 v[24:25], s[4:5], 0, v[48:49]
	v_lshl_add_u64 v[24:25], v[24:25], 0, v[0:1]
	s_mov_b32 s0, 0x43000000
	v_fma_f32 v0, -v29, v32, 1.0
	v_fmac_f32_e32 v32, v0, v32
	v_div_scale_f32 v0, vcc, 1.0, v28, 1.0
	v_mul_f32_e32 v33, v0, v32
	v_fma_f32 v34, -v29, v33, v0
	v_fmac_f32_e32 v33, v34, v32
	v_fma_f32 v0, -v29, v33, v0
	v_div_fmas_f32 v0, v0, v32, v33
	v_div_fixup_f32 v0, v0, v28, 1.0
	v_pk_fma_f32 v[4:5], v[0:1], v[4:5], v[12:13] op_sel_hi:[0,1,1]
	v_pk_fma_f32 v[6:7], v[0:1], v[6:7], v[14:15] op_sel_hi:[0,1,1]
	s_waitcnt vmcnt(0)
	v_pk_fma_f32 v[8:9], v[0:1], v[8:9], v[20:21] op_sel_hi:[0,1,1]
	v_fma_mixlo_f16 v12, v4, s0, 0
	v_pk_fma_f32 v[10:11], v[0:1], v[10:11], v[22:23] op_sel_hi:[0,1,1]
	global_store_dwordx4 v[24:25], v[4:7], off sc1
	global_store_dwordx4 v[24:25], v[8:11], off offset:1024 sc1
	v_mul_f32_e32 v0, 0x43000000, v4
	v_fma_mixlo_f16 v4, v4, s0, -v12 op_sel_hi:[0,0,1]
	v_fma_mixlo_f16 v12, v8, s0, 0
	v_mul_f32_e32 v13, 0x43000000, v8
	v_fma_mixlo_f16 v8, v8, s0, -v12 op_sel_hi:[0,0,1]
	v_mul_f32_e32 v12, 0x43000000, v5
	v_fma_mixlo_f16 v14, v5, s0, 0
	v_cvt_pk_f16_f32 v12, v0, v12
	v_mul_f32_e32 v0, 0x43000000, v9
	v_pk_mul_f32 v[16:17], v[6:7], s[0:1] op_sel_hi:[1,0]
	v_fma_mixhi_f16 v4, v5, s0, -v14 op_sel_hi:[0,0,1]
	v_cvt_pk_f16_f32 v14, v13, v0
	v_cvt_pk_f16_f32 v13, v16, v17
	v_pk_mul_f32 v[18:19], v[10:11], s[0:1] op_sel_hi:[1,0]
	v_cvt_f32_f16_e32 v16, v13
	v_cvt_f32_f16_sdwa v17, v13 dst_sel:DWORD dst_unused:UNUSED_PAD src0_sel:WORD_1
	v_cvt_pk_f16_f32 v15, v18, v19
	v_cvt_f32_f16_e32 v18, v15
	v_cvt_f32_f16_sdwa v19, v15 dst_sel:DWORD dst_unused:UNUSED_PAD src0_sel:WORD_1
	v_fma_mixlo_f16 v5, v9, s0, 0
	v_pk_fma_f32 v[6:7], v[6:7], s[0:1], v[16:17] op_sel_hi:[1,0,1] neg_lo:[0,0,1] neg_hi:[0,0,1]
	v_fma_mixhi_f16 v8, v9, s0, -v5 op_sel_hi:[0,0,1]
	v_cvt_pk_f16_f32 v5, v6, v7
	v_pk_fma_f32 v[6:7], v[10:11], s[0:1], v[18:19] op_sel_hi:[1,0,1] neg_lo:[0,0,1] neg_hi:[0,0,1]
	v_lshlrev_b32_e32 v0, 1, v66
	v_cvt_pk_f16_f32 v9, v6, v7
	v_lshl_add_u64 v[6:7], s[6:7], 0, v[2:3]
	v_lshl_add_u64 v[2:3], s[2:3], 0, v[2:3]
	v_lshl_add_u64 v[6:7], v[6:7], 0, v[0:1]
	v_lshl_add_u64 v[0:1], v[2:3], 0, v[0:1]
	global_store_dwordx2 v[6:7], v[12:13], off
	global_store_dwordx2 v[6:7], v[14:15], off offset:512
	global_store_dwordx2 v[0:1], v[4:5], off
	global_store_dwordx2 v[0:1], v[8:9], off offset:512
	s_endpgm
	s_endpgm
	s_endpgm
	s_endpgm
	s_endpgm
	s_endpgm
	s_endpgm
	s_endpgm
	s_endpgm
	s_endpgm
	s_endpgm
	s_endpgm
	s_endpgm
	s_endpgm
	s_endpgm
	s_endpgm
	s_endpgm
	s_endpgm
	s_endpgm
	s_endpgm
	s_endpgm
	s_endpgm
	s_endpgm
	s_endpgm
	s_endpgm
	s_endpgm
	s_endpgm
	s_endpgm
	s_endpgm
	s_endpgm
	s_endpgm
	s_endpgm
	s_endpgm
	s_endpgm
	s_endpgm
	s_endpgm
	s_endpgm
	s_endpgm
	s_endpgm
	s_endpgm
	s_endpgm
	s_endpgm
	s_endpgm
	s_endpgm
	s_endpgm
	s_endpgm
	s_endpgm
	s_endpgm
	s_endpgm
	s_endpgm
	s_endpgm
	s_endpgm
	s_endpgm
	s_endpgm
	s_endpgm
	s_endpgm
	s_endpgm
	s_endpgm
	.section	.rodata,"a",@progbits
	.p2align	6, 0x0
